# baseline (speedup 1.0000x reference)
_Z12k1_colsum_q8PKfPjPfS2_:
	s_load_dwordx8 s[4:11], s[0:1], 0x0
	v_and_b32_e32 v1, 63, v0
	v_lshrrev_b32_e32 v41, 6, v0
	s_mul_i32 s12, s2, 0xc35
	s_lshr_b32 s12, s12, 4
	v_readfirstlane_b32 s14, v41
	s_add_i32 s13, s2, 1
	s_mul_i32 s13, s13, 0xc35
	s_lshr_b32 s13, s13, 4
	s_sub_u32 s13, s13, s12
	s_sub_u32 s15, s13, 0xc0
	s_cmp_lt_u32 s14, s15
	s_cselect_b32 s29, 1, 0
	v_lshlrev_b32_e32 v34, 4, v1
	v_min_u32_e32 v35, 57, v1
	v_lshlrev_b32_e32 v35, 4, v35
	v_cmp_gt_u32_e64 s[18:19], 58, v1
	s_lshl_b32 s35, s14, 13
	s_add_u32 s36, s35, 0x1000
	v_add_u32_e32 v38, s35, v34
	v_lshrrev_b32_e32 v41, 5, v1
	v_mov_b32_e32 v42, 0xc35000
	v_mul_lo_u32 v39, v41, v42
	v_and_b32_e32 v42, 31, v1
	v_lshl_add_u32 v39, v42, 2, v39
	v_mov_b32_e32 v2, 0
	v_mov_b32_e32 v3, 0
	v_mov_b32_e32 v4, 0
	v_mov_b32_e32 v5, 0
	v_mov_b32_e32 v6, 0
	v_mov_b32_e32 v7, 0
	v_mov_b32_e32 v8, 0
	v_mov_b32_e32 v9, 0
	v_mov_b32_e32 v10, 0
	v_mov_b32_e32 v11, 0
	v_mov_b32_e32 v12, 0
	v_mov_b32_e32 v13, 0
	v_mov_b32_e32 v14, 0
	v_mov_b32_e32 v15, 0
	v_mov_b32_e32 v16, 0
	v_mov_b32_e32 v17, 0
	v_mov_b32_e32 v40, 0
	v_mov_b32_e32 v47, 0x42fe0000
	s_mov_b32 s32, 0x42fe0000
	s_mov_b32 s33, 0xc0c0400
	s_mov_b32 s34, 0x4000c0c
	s_add_u32 s15, s12, s14
	s_mul_i32 s37, s15, 0xfa0
	s_lshl_b32 s15, s15, 7
	s_waitcnt lgkmcnt(0)
	s_add_u32 s16, s4, s37
	s_addc_u32 s17, s5, 0
	s_add_u32 s40, s6, s15
	s_addc_u32 s41, s7, 0
	s_add_u32 s20, s40, 0
	s_addc_u32 s21, s41, 0
	s_add_u32 s22, s20, 0x186a000
	s_addc_u32 s23, s21, 0
	s_add_u32 s24, s22, 0x186a000
	s_addc_u32 s25, s23, 0
	s_add_u32 s26, s24, 0x186a000
	s_addc_u32 s27, s25, 0
	s_mov_b32 m0, s35
	s_nop 0
	global_load_lds_dwordx4 v34, s[16:17] nt
	global_load_lds_dwordx4 v34, s[16:17] offset:1024 nt
	global_load_lds_dwordx4 v34, s[16:17] offset:2048 nt
	global_load_lds_dwordx4 v35, s[16:17] offset:3072 nt
	s_add_u32 s16, s16, 0x7d00
	s_addc_u32 s17, s17, 0
	s_waitcnt vmcnt(0)
	ds_read_b128 v[18:21], v38 offset:0
	ds_read_b128 v[22:25], v38 offset:1024
	ds_read_b128 v[26:29], v38 offset:2048
	ds_read_b128 v[30:33], v38 offset:3072
	s_waitcnt lgkmcnt(0)
	s_mov_b32 m0, s35
	s_nop 0
	global_load_lds_dwordx4 v34, s[16:17] nt
	global_load_lds_dwordx4 v34, s[16:17] offset:1024 nt
	global_load_lds_dwordx4 v34, s[16:17] offset:2048 nt
	global_load_lds_dwordx4 v35, s[16:17] offset:3072 nt
	s_add_u32 s16, s16, 0x7d00
	s_addc_u32 s17, s17, 0
	v_cndmask_b32_e64 v30, 0, v30, s[18:19]
	v_cndmask_b32_e64 v31, 0, v31, s[18:19]
	v_cndmask_b32_e64 v32, 0, v32, s[18:19]
	v_cndmask_b32_e64 v33, 0, v33, s[18:19]
	v_max3_f32 v41, |v18|, |v19|, |v20|
	v_max3_f32 v42, |v21|, |v22|, |v23|
	v_max3_f32 v43, |v24|, |v25|, |v26|
	v_max3_f32 v44, |v27|, |v28|, |v29|
	v_max3_f32 v45, |v30|, |v31|, |v32|
	v_max3_f32 v41, v41, v42, |v33|
	v_max3_f32 v43, v43, v44, v45
	v_max_f32_e32 v41, v41, v43
	v_pk_add_f32 v[2:3], v[2:3], v[18:19]
	v_pk_add_f32 v[4:5], v[4:5], v[20:21]
	v_max_f32_dpp v41, v41, v41 quad_perm:[1,0,3,2] row_mask:0xf bank_mask:0xf
	v_pk_add_f32 v[6:7], v[6:7], v[22:23]
	v_pk_add_f32 v[8:9], v[8:9], v[24:25]
	v_max_f32_dpp v41, v41, v41 quad_perm:[2,3,0,1] row_mask:0xf bank_mask:0xf
	v_pk_add_f32 v[10:11], v[10:11], v[26:27]
	v_pk_add_f32 v[12:13], v[12:13], v[28:29]
	v_max_f32_dpp v41, v41, v41 row_half_mirror row_mask:0xf bank_mask:0xf
	v_pk_add_f32 v[14:15], v[14:15], v[30:31]
	v_pk_add_f32 v[16:17], v[16:17], v[32:33]
	v_max_f32_dpp v41, v41, v41 row_mirror row_mask:0xf bank_mask:0xf
	s_nop 1
	v_max_f32_dpp v41, v41, v41 row_bcast:15 row_mask:0xa bank_mask:0xf
	s_nop 1
	v_max_f32_dpp v41, v41, v41 row_bcast:31 row_mask:0xc bank_mask:0xf
	s_nop 1
	v_readlane_b32 s28, v41, 63
	s_nop 1
	v_div_scale_f32 v48, s[30:31], s28, s28, v47
	v_rcp_f32_e32 v49, v48
	s_nop 0
	v_fma_f32 v50, -v48, v49, 1.0
	v_fmac_f32_e32 v49, v50, v49
	v_mov_b32_e32 v50, s28
	v_div_scale_f32 v50, vcc, s32, v50, s32
	v_mul_f32_e32 v51, v50, v49
	v_fma_f32 v52, -v48, v51, v50
	v_fmac_f32_e32 v51, v52, v49
	v_fma_f32 v48, -v48, v51, v50
	v_div_fmas_f32 v48, v48, v49, v51
	v_div_fixup_f32 v48, v48, s28, v47
	v_cmp_gt_f32_e64 vcc, s28, 0
	v_writelane_b32 v40, s28, 0
	s_nop 0
	v_cndmask_b32_e32 v48, 0, v48, vcc
	v_fmaak_f32 v49, v18, v48, 0x4b400000
	v_fmaak_f32 v50, v19, v48, 0x4b400000
	v_fmaak_f32 v51, v20, v48, 0x4b400000
	v_fmaak_f32 v52, v21, v48, 0x4b400000
	v_perm_b32 v49, v50, v49, s33
	v_perm_b32 v51, v52, v51, s34
	v_or_b32_e32 v56, v49, v51
	v_fmaak_f32 v53, v22, v48, 0x4b400000
	v_fmaak_f32 v54, v23, v48, 0x4b400000
	v_fmaak_f32 v55, v24, v48, 0x4b400000
	v_fmaak_f32 v46, v25, v48, 0x4b400000
	v_perm_b32 v53, v54, v53, s33
	v_perm_b32 v55, v46, v55, s34
	v_or_b32_e32 v57, v53, v55
	v_fmaak_f32 v49, v26, v48, 0x4b400000
	v_fmaak_f32 v50, v27, v48, 0x4b400000
	v_fmaak_f32 v51, v28, v48, 0x4b400000
	v_fmaak_f32 v52, v29, v48, 0x4b400000
	v_perm_b32 v49, v50, v49, s33
	v_perm_b32 v51, v52, v51, s34
	v_or_b32_e32 v58, v49, v51
	v_fmaak_f32 v53, v30, v48, 0x4b400000
	v_fmaak_f32 v54, v31, v48, 0x4b400000
	v_fmaak_f32 v55, v32, v48, 0x4b400000
	v_fmaak_f32 v46, v33, v48, 0x4b400000
	v_perm_b32 v53, v54, v53, s33
	v_perm_b32 v55, v46, v55, s34
	v_or_b32_e32 v59, v53, v55
	s_waitcnt vmcnt(0)
	ds_read_b128 v[18:21], v38 offset:0
	ds_read_b128 v[22:25], v38 offset:1024
	ds_read_b128 v[26:29], v38 offset:2048
	ds_read_b128 v[30:33], v38 offset:3072
	s_waitcnt lgkmcnt(0)
	s_mov_b32 m0, s35
	s_nop 0
	global_load_lds_dwordx4 v34, s[16:17] nt
	global_load_lds_dwordx4 v34, s[16:17] offset:1024 nt
	global_load_lds_dwordx4 v34, s[16:17] offset:2048 nt
	global_load_lds_dwordx4 v35, s[16:17] offset:3072 nt
	s_add_u32 s16, s16, 0x7d00
	s_addc_u32 s17, s17, 0
	v_cndmask_b32_e64 v30, 0, v30, s[18:19]
	v_cndmask_b32_e64 v31, 0, v31, s[18:19]
	v_cndmask_b32_e64 v32, 0, v32, s[18:19]
	v_cndmask_b32_e64 v33, 0, v33, s[18:19]
	v_max3_f32 v41, |v18|, |v19|, |v20|
	v_max3_f32 v42, |v21|, |v22|, |v23|
	v_max3_f32 v43, |v24|, |v25|, |v26|
	v_max3_f32 v44, |v27|, |v28|, |v29|
	v_max3_f32 v45, |v30|, |v31|, |v32|
	v_max3_f32 v41, v41, v42, |v33|
	v_max3_f32 v43, v43, v44, v45
	v_max_f32_e32 v41, v41, v43
	v_pk_add_f32 v[2:3], v[2:3], v[18:19]
	v_pk_add_f32 v[4:5], v[4:5], v[20:21]
	v_max_f32_dpp v41, v41, v41 quad_perm:[1,0,3,2] row_mask:0xf bank_mask:0xf
	v_pk_add_f32 v[6:7], v[6:7], v[22:23]
	v_pk_add_f32 v[8:9], v[8:9], v[24:25]
	v_max_f32_dpp v41, v41, v41 quad_perm:[2,3,0,1] row_mask:0xf bank_mask:0xf
	v_pk_add_f32 v[10:11], v[10:11], v[26:27]
	v_pk_add_f32 v[12:13], v[12:13], v[28:29]
	v_max_f32_dpp v41, v41, v41 row_half_mirror row_mask:0xf bank_mask:0xf
	v_pk_add_f32 v[14:15], v[14:15], v[30:31]
	v_pk_add_f32 v[16:17], v[16:17], v[32:33]
	v_max_f32_dpp v41, v41, v41 row_mirror row_mask:0xf bank_mask:0xf
	s_nop 1
	v_max_f32_dpp v41, v41, v41 row_bcast:15 row_mask:0xa bank_mask:0xf
	s_nop 1
	v_max_f32_dpp v41, v41, v41 row_bcast:31 row_mask:0xc bank_mask:0xf
	s_nop 1
	v_readlane_b32 s28, v41, 63
	s_nop 1
	v_div_scale_f32 v48, s[30:31], s28, s28, v47
	v_rcp_f32_e32 v49, v48
	s_nop 0
	v_fma_f32 v50, -v48, v49, 1.0
	v_fmac_f32_e32 v49, v50, v49
	v_mov_b32_e32 v50, s28
	v_div_scale_f32 v50, vcc, s32, v50, s32
	v_mul_f32_e32 v51, v50, v49
	v_fma_f32 v52, -v48, v51, v50
	v_fmac_f32_e32 v51, v52, v49
	v_fma_f32 v48, -v48, v51, v50
	v_div_fmas_f32 v48, v48, v49, v51
	v_div_fixup_f32 v48, v48, s28, v47
	v_cmp_gt_f32_e64 vcc, s28, 0
	v_writelane_b32 v40, s28, 1
	s_nop 0
	v_cndmask_b32_e32 v48, 0, v48, vcc
	v_fmaak_f32 v49, v18, v48, 0x4b400000
	v_fmaak_f32 v50, v19, v48, 0x4b400000
	v_fmaak_f32 v51, v20, v48, 0x4b400000
	v_fmaak_f32 v52, v21, v48, 0x4b400000
	v_perm_b32 v49, v50, v49, s33
	v_perm_b32 v51, v52, v51, s34
	v_or_b32_e32 v60, v49, v51
	v_fmaak_f32 v53, v22, v48, 0x4b400000
	v_fmaak_f32 v54, v23, v48, 0x4b400000
	v_fmaak_f32 v55, v24, v48, 0x4b400000
	v_fmaak_f32 v46, v25, v48, 0x4b400000
	v_perm_b32 v53, v54, v53, s33
	v_perm_b32 v55, v46, v55, s34
	v_or_b32_e32 v61, v53, v55
	v_fmaak_f32 v49, v26, v48, 0x4b400000
	v_fmaak_f32 v50, v27, v48, 0x4b400000
	v_fmaak_f32 v51, v28, v48, 0x4b400000
	v_fmaak_f32 v52, v29, v48, 0x4b400000
	v_perm_b32 v49, v50, v49, s33
	v_perm_b32 v51, v52, v51, s34
	v_or_b32_e32 v62, v49, v51
	v_fmaak_f32 v53, v30, v48, 0x4b400000
	v_fmaak_f32 v54, v31, v48, 0x4b400000
	v_fmaak_f32 v55, v32, v48, 0x4b400000
	v_fmaak_f32 v46, v33, v48, 0x4b400000
	v_perm_b32 v53, v54, v53, s33
	v_perm_b32 v55, v46, v55, s34
	v_or_b32_e32 v63, v53, v55
	s_waitcnt vmcnt(0)
	ds_read_b128 v[18:21], v38 offset:0
	ds_read_b128 v[22:25], v38 offset:1024
	ds_read_b128 v[26:29], v38 offset:2048
	ds_read_b128 v[30:33], v38 offset:3072
	s_waitcnt lgkmcnt(0)
	s_mov_b32 m0, s35
	s_nop 0
	global_load_lds_dwordx4 v34, s[16:17] nt
	global_load_lds_dwordx4 v34, s[16:17] offset:1024 nt
	global_load_lds_dwordx4 v34, s[16:17] offset:2048 nt
	global_load_lds_dwordx4 v35, s[16:17] offset:3072 nt
	s_add_u32 s16, s16, 0x7d00
	s_addc_u32 s17, s17, 0
	v_cndmask_b32_e64 v30, 0, v30, s[18:19]
	v_cndmask_b32_e64 v31, 0, v31, s[18:19]
	v_cndmask_b32_e64 v32, 0, v32, s[18:19]
	v_cndmask_b32_e64 v33, 0, v33, s[18:19]
	v_max3_f32 v41, |v18|, |v19|, |v20|
	v_max3_f32 v42, |v21|, |v22|, |v23|
	v_max3_f32 v43, |v24|, |v25|, |v26|
	v_max3_f32 v44, |v27|, |v28|, |v29|
	v_max3_f32 v45, |v30|, |v31|, |v32|
	v_max3_f32 v41, v41, v42, |v33|
	v_max3_f32 v43, v43, v44, v45
	v_max_f32_e32 v41, v41, v43
	v_pk_add_f32 v[2:3], v[2:3], v[18:19]
	v_pk_add_f32 v[4:5], v[4:5], v[20:21]
	v_max_f32_dpp v41, v41, v41 quad_perm:[1,0,3,2] row_mask:0xf bank_mask:0xf
	v_pk_add_f32 v[6:7], v[6:7], v[22:23]
	v_pk_add_f32 v[8:9], v[8:9], v[24:25]
	v_max_f32_dpp v41, v41, v41 quad_perm:[2,3,0,1] row_mask:0xf bank_mask:0xf
	v_pk_add_f32 v[10:11], v[10:11], v[26:27]
	v_pk_add_f32 v[12:13], v[12:13], v[28:29]
	v_max_f32_dpp v41, v41, v41 row_half_mirror row_mask:0xf bank_mask:0xf
	v_pk_add_f32 v[14:15], v[14:15], v[30:31]
	v_pk_add_f32 v[16:17], v[16:17], v[32:33]
	v_max_f32_dpp v41, v41, v41 row_mirror row_mask:0xf bank_mask:0xf
	s_nop 1
	v_max_f32_dpp v41, v41, v41 row_bcast:15 row_mask:0xa bank_mask:0xf
	s_nop 1
	v_max_f32_dpp v41, v41, v41 row_bcast:31 row_mask:0xc bank_mask:0xf
	s_nop 1
	v_readlane_b32 s28, v41, 63
	s_nop 1
	v_div_scale_f32 v48, s[30:31], s28, s28, v47
	v_rcp_f32_e32 v49, v48
	s_nop 0
	v_fma_f32 v50, -v48, v49, 1.0
	v_fmac_f32_e32 v49, v50, v49
	v_mov_b32_e32 v50, s28
	v_div_scale_f32 v50, vcc, s32, v50, s32
	v_mul_f32_e32 v51, v50, v49
	v_fma_f32 v52, -v48, v51, v50
	v_fmac_f32_e32 v51, v52, v49
	v_fma_f32 v48, -v48, v51, v50
	v_div_fmas_f32 v48, v48, v49, v51
	v_div_fixup_f32 v48, v48, s28, v47
	v_cmp_gt_f32_e64 vcc, s28, 0
	v_writelane_b32 v40, s28, 2
	s_nop 0
	v_cndmask_b32_e32 v48, 0, v48, vcc
	v_fmaak_f32 v49, v18, v48, 0x4b400000
	v_fmaak_f32 v50, v19, v48, 0x4b400000
	v_fmaak_f32 v51, v20, v48, 0x4b400000
	v_fmaak_f32 v52, v21, v48, 0x4b400000
	v_perm_b32 v49, v50, v49, s33
	v_perm_b32 v51, v52, v51, s34
	v_or_b32_e32 v64, v49, v51
	v_fmaak_f32 v53, v22, v48, 0x4b400000
	v_fmaak_f32 v54, v23, v48, 0x4b400000
	v_fmaak_f32 v55, v24, v48, 0x4b400000
	v_fmaak_f32 v46, v25, v48, 0x4b400000
	v_perm_b32 v53, v54, v53, s33
	v_perm_b32 v55, v46, v55, s34
	v_or_b32_e32 v65, v53, v55
	v_fmaak_f32 v49, v26, v48, 0x4b400000
	v_fmaak_f32 v50, v27, v48, 0x4b400000
	v_fmaak_f32 v51, v28, v48, 0x4b400000
	v_fmaak_f32 v52, v29, v48, 0x4b400000
	v_perm_b32 v49, v50, v49, s33
	v_perm_b32 v51, v52, v51, s34
	v_or_b32_e32 v66, v49, v51
	v_fmaak_f32 v53, v30, v48, 0x4b400000
	v_fmaak_f32 v54, v31, v48, 0x4b400000
	v_fmaak_f32 v55, v32, v48, 0x4b400000
	v_fmaak_f32 v46, v33, v48, 0x4b400000
	v_perm_b32 v53, v54, v53, s33
	v_perm_b32 v55, v46, v55, s34
	v_or_b32_e32 v67, v53, v55
	s_waitcnt vmcnt(0)
	ds_read_b128 v[18:21], v38 offset:0
	ds_read_b128 v[22:25], v38 offset:1024
	ds_read_b128 v[26:29], v38 offset:2048
	ds_read_b128 v[30:33], v38 offset:3072
	s_waitcnt lgkmcnt(0)
	s_mov_b32 m0, s35
	s_nop 0
	global_load_lds_dwordx4 v34, s[16:17] nt
	global_load_lds_dwordx4 v34, s[16:17] offset:1024 nt
	global_load_lds_dwordx4 v34, s[16:17] offset:2048 nt
	global_load_lds_dwordx4 v35, s[16:17] offset:3072 nt
	s_add_u32 s16, s16, 0x7d00
	s_addc_u32 s17, s17, 0
	v_cndmask_b32_e64 v30, 0, v30, s[18:19]
	v_cndmask_b32_e64 v31, 0, v31, s[18:19]
	v_cndmask_b32_e64 v32, 0, v32, s[18:19]
	v_cndmask_b32_e64 v33, 0, v33, s[18:19]
	v_max3_f32 v41, |v18|, |v19|, |v20|
	v_max3_f32 v42, |v21|, |v22|, |v23|
	v_max3_f32 v43, |v24|, |v25|, |v26|
	v_max3_f32 v44, |v27|, |v28|, |v29|
	v_max3_f32 v45, |v30|, |v31|, |v32|
	v_max3_f32 v41, v41, v42, |v33|
	v_max3_f32 v43, v43, v44, v45
	v_max_f32_e32 v41, v41, v43
	v_pk_add_f32 v[2:3], v[2:3], v[18:19]
	v_pk_add_f32 v[4:5], v[4:5], v[20:21]
	v_max_f32_dpp v41, v41, v41 quad_perm:[1,0,3,2] row_mask:0xf bank_mask:0xf
	v_pk_add_f32 v[6:7], v[6:7], v[22:23]
	v_pk_add_f32 v[8:9], v[8:9], v[24:25]
	v_max_f32_dpp v41, v41, v41 quad_perm:[2,3,0,1] row_mask:0xf bank_mask:0xf
	v_pk_add_f32 v[10:11], v[10:11], v[26:27]
	v_pk_add_f32 v[12:13], v[12:13], v[28:29]
	v_max_f32_dpp v41, v41, v41 row_half_mirror row_mask:0xf bank_mask:0xf
	v_pk_add_f32 v[14:15], v[14:15], v[30:31]
	v_pk_add_f32 v[16:17], v[16:17], v[32:33]
	v_max_f32_dpp v41, v41, v41 row_mirror row_mask:0xf bank_mask:0xf
	s_nop 1
	v_max_f32_dpp v41, v41, v41 row_bcast:15 row_mask:0xa bank_mask:0xf
	s_nop 1
	v_max_f32_dpp v41, v41, v41 row_bcast:31 row_mask:0xc bank_mask:0xf
	s_nop 1
	v_readlane_b32 s28, v41, 63
	s_nop 1
	v_div_scale_f32 v48, s[30:31], s28, s28, v47
	v_rcp_f32_e32 v49, v48
	s_nop 0
	v_fma_f32 v50, -v48, v49, 1.0
	v_fmac_f32_e32 v49, v50, v49
	v_mov_b32_e32 v50, s28
	v_div_scale_f32 v50, vcc, s32, v50, s32
	v_mul_f32_e32 v51, v50, v49
	v_fma_f32 v52, -v48, v51, v50
	v_fmac_f32_e32 v51, v52, v49
	v_fma_f32 v48, -v48, v51, v50
	v_div_fmas_f32 v48, v48, v49, v51
	v_div_fixup_f32 v48, v48, s28, v47
	v_cmp_gt_f32_e64 vcc, s28, 0
	v_writelane_b32 v40, s28, 3
	s_nop 0
	v_cndmask_b32_e32 v48, 0, v48, vcc
	v_fmaak_f32 v49, v18, v48, 0x4b400000
	v_fmaak_f32 v50, v19, v48, 0x4b400000
	v_fmaak_f32 v51, v20, v48, 0x4b400000
	v_fmaak_f32 v52, v21, v48, 0x4b400000
	v_perm_b32 v49, v50, v49, s33
	v_perm_b32 v51, v52, v51, s34
	v_or_b32_e32 v68, v49, v51
	v_fmaak_f32 v53, v22, v48, 0x4b400000
	v_fmaak_f32 v54, v23, v48, 0x4b400000
	v_fmaak_f32 v55, v24, v48, 0x4b400000
	v_fmaak_f32 v46, v25, v48, 0x4b400000
	v_perm_b32 v53, v54, v53, s33
	v_perm_b32 v55, v46, v55, s34
	v_or_b32_e32 v69, v53, v55
	v_fmaak_f32 v49, v26, v48, 0x4b400000
	v_fmaak_f32 v50, v27, v48, 0x4b400000
	v_fmaak_f32 v51, v28, v48, 0x4b400000
	v_fmaak_f32 v52, v29, v48, 0x4b400000
	v_perm_b32 v49, v50, v49, s33
	v_perm_b32 v51, v52, v51, s34
	v_or_b32_e32 v70, v49, v51
	v_fmaak_f32 v53, v30, v48, 0x4b400000
	v_fmaak_f32 v54, v31, v48, 0x4b400000
	v_fmaak_f32 v55, v32, v48, 0x4b400000
	v_fmaak_f32 v46, v33, v48, 0x4b400000
	v_perm_b32 v53, v54, v53, s33
	v_perm_b32 v55, v46, v55, s34
	v_or_b32_e32 v71, v53, v55
	s_waitcnt vmcnt(0)
	ds_read_b128 v[18:21], v38 offset:0
	ds_read_b128 v[22:25], v38 offset:1024
	ds_read_b128 v[26:29], v38 offset:2048
	ds_read_b128 v[30:33], v38 offset:3072
	s_waitcnt lgkmcnt(0)
	s_mov_b32 m0, s35
	s_nop 0
	global_load_lds_dwordx4 v34, s[16:17] nt
	global_load_lds_dwordx4 v34, s[16:17] offset:1024 nt
	global_load_lds_dwordx4 v34, s[16:17] offset:2048 nt
	global_load_lds_dwordx4 v35, s[16:17] offset:3072 nt
	s_add_u32 s16, s16, 0x7d00
	s_addc_u32 s17, s17, 0
	v_cndmask_b32_e64 v30, 0, v30, s[18:19]
	v_cndmask_b32_e64 v31, 0, v31, s[18:19]
	v_cndmask_b32_e64 v32, 0, v32, s[18:19]
	v_cndmask_b32_e64 v33, 0, v33, s[18:19]
	v_max3_f32 v41, |v18|, |v19|, |v20|
	v_max3_f32 v42, |v21|, |v22|, |v23|
	v_max3_f32 v43, |v24|, |v25|, |v26|
	v_max3_f32 v44, |v27|, |v28|, |v29|
	v_max3_f32 v45, |v30|, |v31|, |v32|
	v_max3_f32 v41, v41, v42, |v33|
	v_max3_f32 v43, v43, v44, v45
	v_max_f32_e32 v41, v41, v43
	v_pk_add_f32 v[2:3], v[2:3], v[18:19]
	v_pk_add_f32 v[4:5], v[4:5], v[20:21]
	v_max_f32_dpp v41, v41, v41 quad_perm:[1,0,3,2] row_mask:0xf bank_mask:0xf
	v_pk_add_f32 v[6:7], v[6:7], v[22:23]
	v_pk_add_f32 v[8:9], v[8:9], v[24:25]
	v_max_f32_dpp v41, v41, v41 quad_perm:[2,3,0,1] row_mask:0xf bank_mask:0xf
	v_pk_add_f32 v[10:11], v[10:11], v[26:27]
	v_pk_add_f32 v[12:13], v[12:13], v[28:29]
	v_max_f32_dpp v41, v41, v41 row_half_mirror row_mask:0xf bank_mask:0xf
	v_pk_add_f32 v[14:15], v[14:15], v[30:31]
	v_pk_add_f32 v[16:17], v[16:17], v[32:33]
	v_max_f32_dpp v41, v41, v41 row_mirror row_mask:0xf bank_mask:0xf
	s_nop 1
	v_max_f32_dpp v41, v41, v41 row_bcast:15 row_mask:0xa bank_mask:0xf
	s_nop 1
	v_max_f32_dpp v41, v41, v41 row_bcast:31 row_mask:0xc bank_mask:0xf
	s_nop 1
	v_readlane_b32 s28, v41, 63
	s_nop 1
	v_div_scale_f32 v48, s[30:31], s28, s28, v47
	v_rcp_f32_e32 v49, v48
	s_nop 0
	v_fma_f32 v50, -v48, v49, 1.0
	v_fmac_f32_e32 v49, v50, v49
	v_mov_b32_e32 v50, s28
	v_div_scale_f32 v50, vcc, s32, v50, s32
	v_mul_f32_e32 v51, v50, v49
	v_fma_f32 v52, -v48, v51, v50
	v_fmac_f32_e32 v51, v52, v49
	v_fma_f32 v48, -v48, v51, v50
	v_div_fmas_f32 v48, v48, v49, v51
	v_div_fixup_f32 v48, v48, s28, v47
	v_cmp_gt_f32_e64 vcc, s28, 0
	v_writelane_b32 v40, s28, 4
	s_nop 0
	v_cndmask_b32_e32 v48, 0, v48, vcc
	v_fmaak_f32 v49, v18, v48, 0x4b400000
	v_fmaak_f32 v50, v19, v48, 0x4b400000
	v_fmaak_f32 v51, v20, v48, 0x4b400000
	v_fmaak_f32 v52, v21, v48, 0x4b400000
	v_perm_b32 v49, v50, v49, s33
	v_perm_b32 v51, v52, v51, s34
	v_or_b32_e32 v72, v49, v51
	v_fmaak_f32 v53, v22, v48, 0x4b400000
	v_fmaak_f32 v54, v23, v48, 0x4b400000
	v_fmaak_f32 v55, v24, v48, 0x4b400000
	v_fmaak_f32 v46, v25, v48, 0x4b400000
	v_perm_b32 v53, v54, v53, s33
	v_perm_b32 v55, v46, v55, s34
	v_or_b32_e32 v73, v53, v55
	v_fmaak_f32 v49, v26, v48, 0x4b400000
	v_fmaak_f32 v50, v27, v48, 0x4b400000
	v_fmaak_f32 v51, v28, v48, 0x4b400000
	v_fmaak_f32 v52, v29, v48, 0x4b400000
	v_perm_b32 v49, v50, v49, s33
	v_perm_b32 v51, v52, v51, s34
	v_or_b32_e32 v74, v49, v51
	v_fmaak_f32 v53, v30, v48, 0x4b400000
	v_fmaak_f32 v54, v31, v48, 0x4b400000
	v_fmaak_f32 v55, v32, v48, 0x4b400000
	v_fmaak_f32 v46, v33, v48, 0x4b400000
	v_perm_b32 v53, v54, v53, s33
	v_perm_b32 v55, v46, v55, s34
	v_or_b32_e32 v75, v53, v55
	s_waitcnt vmcnt(0)
	ds_read_b128 v[18:21], v38 offset:0
	ds_read_b128 v[22:25], v38 offset:1024
	ds_read_b128 v[26:29], v38 offset:2048
	ds_read_b128 v[30:33], v38 offset:3072
	s_waitcnt lgkmcnt(0)
	s_mov_b32 m0, s35
	s_nop 0
	global_load_lds_dwordx4 v34, s[16:17] nt
	global_load_lds_dwordx4 v34, s[16:17] offset:1024 nt
	global_load_lds_dwordx4 v34, s[16:17] offset:2048 nt
	global_load_lds_dwordx4 v35, s[16:17] offset:3072 nt
	s_add_u32 s16, s16, 0x7d00
	s_addc_u32 s17, s17, 0
	v_cndmask_b32_e64 v30, 0, v30, s[18:19]
	v_cndmask_b32_e64 v31, 0, v31, s[18:19]
	v_cndmask_b32_e64 v32, 0, v32, s[18:19]
	v_cndmask_b32_e64 v33, 0, v33, s[18:19]
	v_max3_f32 v41, |v18|, |v19|, |v20|
	v_max3_f32 v42, |v21|, |v22|, |v23|
	v_max3_f32 v43, |v24|, |v25|, |v26|
	v_max3_f32 v44, |v27|, |v28|, |v29|
	v_max3_f32 v45, |v30|, |v31|, |v32|
	v_max3_f32 v41, v41, v42, |v33|
	v_max3_f32 v43, v43, v44, v45
	v_max_f32_e32 v41, v41, v43
	v_pk_add_f32 v[2:3], v[2:3], v[18:19]
	v_pk_add_f32 v[4:5], v[4:5], v[20:21]
	v_max_f32_dpp v41, v41, v41 quad_perm:[1,0,3,2] row_mask:0xf bank_mask:0xf
	v_pk_add_f32 v[6:7], v[6:7], v[22:23]
	v_pk_add_f32 v[8:9], v[8:9], v[24:25]
	v_max_f32_dpp v41, v41, v41 quad_perm:[2,3,0,1] row_mask:0xf bank_mask:0xf
	v_pk_add_f32 v[10:11], v[10:11], v[26:27]
	v_pk_add_f32 v[12:13], v[12:13], v[28:29]
	v_max_f32_dpp v41, v41, v41 row_half_mirror row_mask:0xf bank_mask:0xf
	v_pk_add_f32 v[14:15], v[14:15], v[30:31]
	v_pk_add_f32 v[16:17], v[16:17], v[32:33]
	v_max_f32_dpp v41, v41, v41 row_mirror row_mask:0xf bank_mask:0xf
	s_nop 1
	v_max_f32_dpp v41, v41, v41 row_bcast:15 row_mask:0xa bank_mask:0xf
	s_nop 1
	v_max_f32_dpp v41, v41, v41 row_bcast:31 row_mask:0xc bank_mask:0xf
	s_nop 1
	v_readlane_b32 s28, v41, 63
	s_nop 1
	v_div_scale_f32 v48, s[30:31], s28, s28, v47
	v_rcp_f32_e32 v49, v48
	s_nop 0
	v_fma_f32 v50, -v48, v49, 1.0
	v_fmac_f32_e32 v49, v50, v49
	v_mov_b32_e32 v50, s28
	v_div_scale_f32 v50, vcc, s32, v50, s32
	v_mul_f32_e32 v51, v50, v49
	v_fma_f32 v52, -v48, v51, v50
	v_fmac_f32_e32 v51, v52, v49
	v_fma_f32 v48, -v48, v51, v50
	v_div_fmas_f32 v48, v48, v49, v51
	v_div_fixup_f32 v48, v48, s28, v47
	v_cmp_gt_f32_e64 vcc, s28, 0
	v_writelane_b32 v40, s28, 5
	s_nop 0
	v_cndmask_b32_e32 v48, 0, v48, vcc
	v_fmaak_f32 v49, v18, v48, 0x4b400000
	v_fmaak_f32 v50, v19, v48, 0x4b400000
	v_fmaak_f32 v51, v20, v48, 0x4b400000
	v_fmaak_f32 v52, v21, v48, 0x4b400000
	v_perm_b32 v49, v50, v49, s33
	v_perm_b32 v51, v52, v51, s34
	v_or_b32_e32 v76, v49, v51
	v_fmaak_f32 v53, v22, v48, 0x4b400000
	v_fmaak_f32 v54, v23, v48, 0x4b400000
	v_fmaak_f32 v55, v24, v48, 0x4b400000
	v_fmaak_f32 v46, v25, v48, 0x4b400000
	v_perm_b32 v53, v54, v53, s33
	v_perm_b32 v55, v46, v55, s34
	v_or_b32_e32 v77, v53, v55
	v_fmaak_f32 v49, v26, v48, 0x4b400000
	v_fmaak_f32 v50, v27, v48, 0x4b400000
	v_fmaak_f32 v51, v28, v48, 0x4b400000
	v_fmaak_f32 v52, v29, v48, 0x4b400000
	v_perm_b32 v49, v50, v49, s33
	v_perm_b32 v51, v52, v51, s34
	v_or_b32_e32 v78, v49, v51
	v_fmaak_f32 v53, v30, v48, 0x4b400000
	v_fmaak_f32 v54, v31, v48, 0x4b400000
	v_fmaak_f32 v55, v32, v48, 0x4b400000
	v_fmaak_f32 v46, v33, v48, 0x4b400000
	v_perm_b32 v53, v54, v53, s33
	v_perm_b32 v55, v46, v55, s34
	v_or_b32_e32 v79, v53, v55
	s_waitcnt vmcnt(0)
	ds_read_b128 v[18:21], v38 offset:0
	ds_read_b128 v[22:25], v38 offset:1024
	ds_read_b128 v[26:29], v38 offset:2048
	ds_read_b128 v[30:33], v38 offset:3072
	s_waitcnt lgkmcnt(0)
	s_mov_b32 m0, s35
	s_nop 0
	global_load_lds_dwordx4 v34, s[16:17] nt
	global_load_lds_dwordx4 v34, s[16:17] offset:1024 nt
	global_load_lds_dwordx4 v34, s[16:17] offset:2048 nt
	global_load_lds_dwordx4 v35, s[16:17] offset:3072 nt
	s_add_u32 s16, s16, 0x7d00
	s_addc_u32 s17, s17, 0
	v_cndmask_b32_e64 v30, 0, v30, s[18:19]
	v_cndmask_b32_e64 v31, 0, v31, s[18:19]
	v_cndmask_b32_e64 v32, 0, v32, s[18:19]
	v_cndmask_b32_e64 v33, 0, v33, s[18:19]
	v_max3_f32 v41, |v18|, |v19|, |v20|
	v_max3_f32 v42, |v21|, |v22|, |v23|
	v_max3_f32 v43, |v24|, |v25|, |v26|
	v_max3_f32 v44, |v27|, |v28|, |v29|
	v_max3_f32 v45, |v30|, |v31|, |v32|
	v_max3_f32 v41, v41, v42, |v33|
	v_max3_f32 v43, v43, v44, v45
	v_max_f32_e32 v41, v41, v43
	v_pk_add_f32 v[2:3], v[2:3], v[18:19]
	v_pk_add_f32 v[4:5], v[4:5], v[20:21]
	v_max_f32_dpp v41, v41, v41 quad_perm:[1,0,3,2] row_mask:0xf bank_mask:0xf
	v_pk_add_f32 v[6:7], v[6:7], v[22:23]
	v_pk_add_f32 v[8:9], v[8:9], v[24:25]
	v_max_f32_dpp v41, v41, v41 quad_perm:[2,3,0,1] row_mask:0xf bank_mask:0xf
	v_pk_add_f32 v[10:11], v[10:11], v[26:27]
	v_pk_add_f32 v[12:13], v[12:13], v[28:29]
	v_max_f32_dpp v41, v41, v41 row_half_mirror row_mask:0xf bank_mask:0xf
	v_pk_add_f32 v[14:15], v[14:15], v[30:31]
	v_pk_add_f32 v[16:17], v[16:17], v[32:33]
	v_max_f32_dpp v41, v41, v41 row_mirror row_mask:0xf bank_mask:0xf
	s_nop 1
	v_max_f32_dpp v41, v41, v41 row_bcast:15 row_mask:0xa bank_mask:0xf
	s_nop 1
	v_max_f32_dpp v41, v41, v41 row_bcast:31 row_mask:0xc bank_mask:0xf
	s_nop 1
	v_readlane_b32 s28, v41, 63
	s_nop 1
	v_div_scale_f32 v48, s[30:31], s28, s28, v47
	v_rcp_f32_e32 v49, v48
	s_nop 0
	v_fma_f32 v50, -v48, v49, 1.0
	v_fmac_f32_e32 v49, v50, v49
	v_mov_b32_e32 v50, s28
	v_div_scale_f32 v50, vcc, s32, v50, s32
	v_mul_f32_e32 v51, v50, v49
	v_fma_f32 v52, -v48, v51, v50
	v_fmac_f32_e32 v51, v52, v49
	v_fma_f32 v48, -v48, v51, v50
	v_div_fmas_f32 v48, v48, v49, v51
	v_div_fixup_f32 v48, v48, s28, v47
	v_cmp_gt_f32_e64 vcc, s28, 0
	v_writelane_b32 v40, s28, 6
	s_nop 0
	v_cndmask_b32_e32 v48, 0, v48, vcc
	v_fmaak_f32 v49, v18, v48, 0x4b400000
	v_fmaak_f32 v50, v19, v48, 0x4b400000
	v_fmaak_f32 v51, v20, v48, 0x4b400000
	v_fmaak_f32 v52, v21, v48, 0x4b400000
	v_perm_b32 v49, v50, v49, s33
	v_perm_b32 v51, v52, v51, s34
	v_or_b32_e32 v80, v49, v51
	v_fmaak_f32 v53, v22, v48, 0x4b400000
	v_fmaak_f32 v54, v23, v48, 0x4b400000
	v_fmaak_f32 v55, v24, v48, 0x4b400000
	v_fmaak_f32 v46, v25, v48, 0x4b400000
	v_perm_b32 v53, v54, v53, s33
	v_perm_b32 v55, v46, v55, s34
	v_or_b32_e32 v81, v53, v55
	v_fmaak_f32 v49, v26, v48, 0x4b400000
	v_fmaak_f32 v50, v27, v48, 0x4b400000
	v_fmaak_f32 v51, v28, v48, 0x4b400000
	v_fmaak_f32 v52, v29, v48, 0x4b400000
	v_perm_b32 v49, v50, v49, s33
	v_perm_b32 v51, v52, v51, s34
	v_or_b32_e32 v82, v49, v51
	v_fmaak_f32 v53, v30, v48, 0x4b400000
	v_fmaak_f32 v54, v31, v48, 0x4b400000
	v_fmaak_f32 v55, v32, v48, 0x4b400000
	v_fmaak_f32 v46, v33, v48, 0x4b400000
	v_perm_b32 v53, v54, v53, s33
	v_perm_b32 v55, v46, v55, s34
	v_or_b32_e32 v83, v53, v55
	s_waitcnt vmcnt(0)
	ds_read_b128 v[18:21], v38 offset:0
	ds_read_b128 v[22:25], v38 offset:1024
	ds_read_b128 v[26:29], v38 offset:2048
	ds_read_b128 v[30:33], v38 offset:3072
	s_waitcnt lgkmcnt(0)
	s_mov_b32 m0, s35
	s_nop 0
	global_load_lds_dwordx4 v34, s[16:17] nt
	global_load_lds_dwordx4 v34, s[16:17] offset:1024 nt
	global_load_lds_dwordx4 v34, s[16:17] offset:2048 nt
	global_load_lds_dwordx4 v35, s[16:17] offset:3072 nt
	s_add_u32 s16, s16, 0x7d00
	s_addc_u32 s17, s17, 0
	v_cndmask_b32_e64 v30, 0, v30, s[18:19]
	v_cndmask_b32_e64 v31, 0, v31, s[18:19]
	v_cndmask_b32_e64 v32, 0, v32, s[18:19]
	v_cndmask_b32_e64 v33, 0, v33, s[18:19]
	v_max3_f32 v41, |v18|, |v19|, |v20|
	v_max3_f32 v42, |v21|, |v22|, |v23|
	v_max3_f32 v43, |v24|, |v25|, |v26|
	v_max3_f32 v44, |v27|, |v28|, |v29|
	v_max3_f32 v45, |v30|, |v31|, |v32|
	v_max3_f32 v41, v41, v42, |v33|
	v_max3_f32 v43, v43, v44, v45
	v_max_f32_e32 v41, v41, v43
	v_pk_add_f32 v[2:3], v[2:3], v[18:19]
	v_pk_add_f32 v[4:5], v[4:5], v[20:21]
	v_max_f32_dpp v41, v41, v41 quad_perm:[1,0,3,2] row_mask:0xf bank_mask:0xf
	v_pk_add_f32 v[6:7], v[6:7], v[22:23]
	v_pk_add_f32 v[8:9], v[8:9], v[24:25]
	v_max_f32_dpp v41, v41, v41 quad_perm:[2,3,0,1] row_mask:0xf bank_mask:0xf
	v_pk_add_f32 v[10:11], v[10:11], v[26:27]
	v_pk_add_f32 v[12:13], v[12:13], v[28:29]
	v_max_f32_dpp v41, v41, v41 row_half_mirror row_mask:0xf bank_mask:0xf
	v_pk_add_f32 v[14:15], v[14:15], v[30:31]
	v_pk_add_f32 v[16:17], v[16:17], v[32:33]
	v_max_f32_dpp v41, v41, v41 row_mirror row_mask:0xf bank_mask:0xf
	s_nop 1
	v_max_f32_dpp v41, v41, v41 row_bcast:15 row_mask:0xa bank_mask:0xf
	s_nop 1
	v_max_f32_dpp v41, v41, v41 row_bcast:31 row_mask:0xc bank_mask:0xf
	s_nop 1
	v_readlane_b32 s28, v41, 63
	s_nop 1
	v_div_scale_f32 v48, s[30:31], s28, s28, v47
	v_rcp_f32_e32 v49, v48
	s_nop 0
	v_fma_f32 v50, -v48, v49, 1.0
	v_fmac_f32_e32 v49, v50, v49
	v_mov_b32_e32 v50, s28
	v_div_scale_f32 v50, vcc, s32, v50, s32
	v_mul_f32_e32 v51, v50, v49
	v_fma_f32 v52, -v48, v51, v50
	v_fmac_f32_e32 v51, v52, v49
	v_fma_f32 v48, -v48, v51, v50
	v_div_fmas_f32 v48, v48, v49, v51
	v_div_fixup_f32 v48, v48, s28, v47
	v_cmp_gt_f32_e64 vcc, s28, 0
	v_writelane_b32 v40, s28, 7
	s_nop 0
	v_cndmask_b32_e32 v48, 0, v48, vcc
	v_fmaak_f32 v49, v18, v48, 0x4b400000
	v_fmaak_f32 v50, v19, v48, 0x4b400000
	v_fmaak_f32 v51, v20, v48, 0x4b400000
	v_fmaak_f32 v52, v21, v48, 0x4b400000
	v_perm_b32 v49, v50, v49, s33
	v_perm_b32 v51, v52, v51, s34
	v_or_b32_e32 v84, v49, v51
	v_fmaak_f32 v53, v22, v48, 0x4b400000
	v_fmaak_f32 v54, v23, v48, 0x4b400000
	v_fmaak_f32 v55, v24, v48, 0x4b400000
	v_fmaak_f32 v46, v25, v48, 0x4b400000
	v_perm_b32 v53, v54, v53, s33
	v_perm_b32 v55, v46, v55, s34
	v_or_b32_e32 v85, v53, v55
	v_fmaak_f32 v49, v26, v48, 0x4b400000
	v_fmaak_f32 v50, v27, v48, 0x4b400000
	v_fmaak_f32 v51, v28, v48, 0x4b400000
	v_fmaak_f32 v52, v29, v48, 0x4b400000
	v_perm_b32 v49, v50, v49, s33
	v_perm_b32 v51, v52, v51, s34
	v_or_b32_e32 v86, v49, v51
	v_fmaak_f32 v53, v30, v48, 0x4b400000
	v_fmaak_f32 v54, v31, v48, 0x4b400000
	v_fmaak_f32 v55, v32, v48, 0x4b400000
	v_fmaak_f32 v46, v33, v48, 0x4b400000
	v_perm_b32 v53, v54, v53, s33
	v_perm_b32 v55, v46, v55, s34
	v_or_b32_e32 v87, v53, v55
	s_waitcnt vmcnt(0)
	ds_read_b128 v[18:21], v38 offset:0
	ds_read_b128 v[22:25], v38 offset:1024
	ds_read_b128 v[26:29], v38 offset:2048
	ds_read_b128 v[30:33], v38 offset:3072
	s_waitcnt lgkmcnt(0)
	s_mov_b32 m0, s35
	s_nop 0
	global_load_lds_dwordx4 v34, s[16:17] nt
	global_load_lds_dwordx4 v34, s[16:17] offset:1024 nt
	global_load_lds_dwordx4 v34, s[16:17] offset:2048 nt
	global_load_lds_dwordx4 v35, s[16:17] offset:3072 nt
	s_add_u32 s16, s16, 0x7d00
	s_addc_u32 s17, s17, 0
	v_cndmask_b32_e64 v30, 0, v30, s[18:19]
	v_cndmask_b32_e64 v31, 0, v31, s[18:19]
	v_cndmask_b32_e64 v32, 0, v32, s[18:19]
	v_cndmask_b32_e64 v33, 0, v33, s[18:19]
	v_max3_f32 v41, |v18|, |v19|, |v20|
	v_max3_f32 v42, |v21|, |v22|, |v23|
	v_max3_f32 v43, |v24|, |v25|, |v26|
	v_max3_f32 v44, |v27|, |v28|, |v29|
	v_max3_f32 v45, |v30|, |v31|, |v32|
	v_max3_f32 v41, v41, v42, |v33|
	v_max3_f32 v43, v43, v44, v45
	v_max_f32_e32 v41, v41, v43
	v_pk_add_f32 v[2:3], v[2:3], v[18:19]
	v_pk_add_f32 v[4:5], v[4:5], v[20:21]
	v_max_f32_dpp v41, v41, v41 quad_perm:[1,0,3,2] row_mask:0xf bank_mask:0xf
	v_pk_add_f32 v[6:7], v[6:7], v[22:23]
	v_pk_add_f32 v[8:9], v[8:9], v[24:25]
	v_max_f32_dpp v41, v41, v41 quad_perm:[2,3,0,1] row_mask:0xf bank_mask:0xf
	v_pk_add_f32 v[10:11], v[10:11], v[26:27]
	v_pk_add_f32 v[12:13], v[12:13], v[28:29]
	v_max_f32_dpp v41, v41, v41 row_half_mirror row_mask:0xf bank_mask:0xf
	v_pk_add_f32 v[14:15], v[14:15], v[30:31]
	v_pk_add_f32 v[16:17], v[16:17], v[32:33]
	v_max_f32_dpp v41, v41, v41 row_mirror row_mask:0xf bank_mask:0xf
	s_nop 1
	v_max_f32_dpp v41, v41, v41 row_bcast:15 row_mask:0xa bank_mask:0xf
	s_nop 1
	v_max_f32_dpp v41, v41, v41 row_bcast:31 row_mask:0xc bank_mask:0xf
	s_nop 1
	v_readlane_b32 s28, v41, 63
	s_nop 1
	v_div_scale_f32 v48, s[30:31], s28, s28, v47
	v_rcp_f32_e32 v49, v48
	s_nop 0
	v_fma_f32 v50, -v48, v49, 1.0
	v_fmac_f32_e32 v49, v50, v49
	v_mov_b32_e32 v50, s28
	v_div_scale_f32 v50, vcc, s32, v50, s32
	v_mul_f32_e32 v51, v50, v49
	v_fma_f32 v52, -v48, v51, v50
	v_fmac_f32_e32 v51, v52, v49
	v_fma_f32 v48, -v48, v51, v50
	v_div_fmas_f32 v48, v48, v49, v51
	v_div_fixup_f32 v48, v48, s28, v47
	v_cmp_gt_f32_e64 vcc, s28, 0
	v_writelane_b32 v40, s28, 8
	s_nop 0
	v_cndmask_b32_e32 v48, 0, v48, vcc
	v_fmaak_f32 v49, v18, v48, 0x4b400000
	v_fmaak_f32 v50, v19, v48, 0x4b400000
	v_fmaak_f32 v51, v20, v48, 0x4b400000
	v_fmaak_f32 v52, v21, v48, 0x4b400000
	v_perm_b32 v49, v50, v49, s33
	v_perm_b32 v51, v52, v51, s34
	v_or_b32_e32 v88, v49, v51
	v_fmaak_f32 v53, v22, v48, 0x4b400000
	v_fmaak_f32 v54, v23, v48, 0x4b400000
	v_fmaak_f32 v55, v24, v48, 0x4b400000
	v_fmaak_f32 v46, v25, v48, 0x4b400000
	v_perm_b32 v53, v54, v53, s33
	v_perm_b32 v55, v46, v55, s34
	v_or_b32_e32 v89, v53, v55
	v_fmaak_f32 v49, v26, v48, 0x4b400000
	v_fmaak_f32 v50, v27, v48, 0x4b400000
	v_fmaak_f32 v51, v28, v48, 0x4b400000
	v_fmaak_f32 v52, v29, v48, 0x4b400000
	v_perm_b32 v49, v50, v49, s33
	v_perm_b32 v51, v52, v51, s34
	v_or_b32_e32 v90, v49, v51
	v_fmaak_f32 v53, v30, v48, 0x4b400000
	v_fmaak_f32 v54, v31, v48, 0x4b400000
	v_fmaak_f32 v55, v32, v48, 0x4b400000
	v_fmaak_f32 v46, v33, v48, 0x4b400000
	v_perm_b32 v53, v54, v53, s33
	v_perm_b32 v55, v46, v55, s34
	v_or_b32_e32 v91, v53, v55
	s_waitcnt vmcnt(0)
	ds_read_b128 v[18:21], v38 offset:0
	ds_read_b128 v[22:25], v38 offset:1024
	ds_read_b128 v[26:29], v38 offset:2048
	ds_read_b128 v[30:33], v38 offset:3072
	s_waitcnt lgkmcnt(0)
	s_mov_b32 m0, s35
	s_nop 0
	global_load_lds_dwordx4 v34, s[16:17] nt
	global_load_lds_dwordx4 v34, s[16:17] offset:1024 nt
	global_load_lds_dwordx4 v34, s[16:17] offset:2048 nt
	global_load_lds_dwordx4 v35, s[16:17] offset:3072 nt
	s_add_u32 s16, s16, 0x7d00
	s_addc_u32 s17, s17, 0
	v_cndmask_b32_e64 v30, 0, v30, s[18:19]
	v_cndmask_b32_e64 v31, 0, v31, s[18:19]
	v_cndmask_b32_e64 v32, 0, v32, s[18:19]
	v_cndmask_b32_e64 v33, 0, v33, s[18:19]
	v_max3_f32 v41, |v18|, |v19|, |v20|
	v_max3_f32 v42, |v21|, |v22|, |v23|
	v_max3_f32 v43, |v24|, |v25|, |v26|
	v_max3_f32 v44, |v27|, |v28|, |v29|
	v_max3_f32 v45, |v30|, |v31|, |v32|
	v_max3_f32 v41, v41, v42, |v33|
	v_max3_f32 v43, v43, v44, v45
	v_max_f32_e32 v41, v41, v43
	v_pk_add_f32 v[2:3], v[2:3], v[18:19]
	v_pk_add_f32 v[4:5], v[4:5], v[20:21]
	v_max_f32_dpp v41, v41, v41 quad_perm:[1,0,3,2] row_mask:0xf bank_mask:0xf
	v_pk_add_f32 v[6:7], v[6:7], v[22:23]
	v_pk_add_f32 v[8:9], v[8:9], v[24:25]
	v_max_f32_dpp v41, v41, v41 quad_perm:[2,3,0,1] row_mask:0xf bank_mask:0xf
	v_pk_add_f32 v[10:11], v[10:11], v[26:27]
	v_pk_add_f32 v[12:13], v[12:13], v[28:29]
	v_max_f32_dpp v41, v41, v41 row_half_mirror row_mask:0xf bank_mask:0xf
	v_pk_add_f32 v[14:15], v[14:15], v[30:31]
	v_pk_add_f32 v[16:17], v[16:17], v[32:33]
	v_max_f32_dpp v41, v41, v41 row_mirror row_mask:0xf bank_mask:0xf
	s_nop 1
	v_max_f32_dpp v41, v41, v41 row_bcast:15 row_mask:0xa bank_mask:0xf
	s_nop 1
	v_max_f32_dpp v41, v41, v41 row_bcast:31 row_mask:0xc bank_mask:0xf
	s_nop 1
	v_readlane_b32 s28, v41, 63
	s_nop 1
	v_div_scale_f32 v48, s[30:31], s28, s28, v47
	v_rcp_f32_e32 v49, v48
	s_nop 0
	v_fma_f32 v50, -v48, v49, 1.0
	v_fmac_f32_e32 v49, v50, v49
	v_mov_b32_e32 v50, s28
	v_div_scale_f32 v50, vcc, s32, v50, s32
	v_mul_f32_e32 v51, v50, v49
	v_fma_f32 v52, -v48, v51, v50
	v_fmac_f32_e32 v51, v52, v49
	v_fma_f32 v48, -v48, v51, v50
	v_div_fmas_f32 v48, v48, v49, v51
	v_div_fixup_f32 v48, v48, s28, v47
	v_cmp_gt_f32_e64 vcc, s28, 0
	v_writelane_b32 v40, s28, 9
	s_nop 0
	v_cndmask_b32_e32 v48, 0, v48, vcc
	v_fmaak_f32 v49, v18, v48, 0x4b400000
	v_fmaak_f32 v50, v19, v48, 0x4b400000
	v_fmaak_f32 v51, v20, v48, 0x4b400000
	v_fmaak_f32 v52, v21, v48, 0x4b400000
	v_perm_b32 v49, v50, v49, s33
	v_perm_b32 v51, v52, v51, s34
	v_or_b32_e32 v92, v49, v51
	v_fmaak_f32 v53, v22, v48, 0x4b400000
	v_fmaak_f32 v54, v23, v48, 0x4b400000
	v_fmaak_f32 v55, v24, v48, 0x4b400000
	v_fmaak_f32 v46, v25, v48, 0x4b400000
	v_perm_b32 v53, v54, v53, s33
	v_perm_b32 v55, v46, v55, s34
	v_or_b32_e32 v93, v53, v55
	v_fmaak_f32 v49, v26, v48, 0x4b400000
	v_fmaak_f32 v50, v27, v48, 0x4b400000
	v_fmaak_f32 v51, v28, v48, 0x4b400000
	v_fmaak_f32 v52, v29, v48, 0x4b400000
	v_perm_b32 v49, v50, v49, s33
	v_perm_b32 v51, v52, v51, s34
	v_or_b32_e32 v94, v49, v51
	v_fmaak_f32 v53, v30, v48, 0x4b400000
	v_fmaak_f32 v54, v31, v48, 0x4b400000
	v_fmaak_f32 v55, v32, v48, 0x4b400000
	v_fmaak_f32 v46, v33, v48, 0x4b400000
	v_perm_b32 v53, v54, v53, s33
	v_perm_b32 v55, v46, v55, s34
	v_or_b32_e32 v95, v53, v55
	s_waitcnt vmcnt(0)
	ds_read_b128 v[18:21], v38 offset:0
	ds_read_b128 v[22:25], v38 offset:1024
	ds_read_b128 v[26:29], v38 offset:2048
	ds_read_b128 v[30:33], v38 offset:3072
	s_waitcnt lgkmcnt(0)
	s_mov_b32 m0, s35
	s_nop 0
	global_load_lds_dwordx4 v34, s[16:17] nt
	global_load_lds_dwordx4 v34, s[16:17] offset:1024 nt
	global_load_lds_dwordx4 v34, s[16:17] offset:2048 nt
	global_load_lds_dwordx4 v35, s[16:17] offset:3072 nt
	s_add_u32 s16, s16, 0x7d00
	s_addc_u32 s17, s17, 0
	v_cndmask_b32_e64 v30, 0, v30, s[18:19]
	v_cndmask_b32_e64 v31, 0, v31, s[18:19]
	v_cndmask_b32_e64 v32, 0, v32, s[18:19]
	v_cndmask_b32_e64 v33, 0, v33, s[18:19]
	v_max3_f32 v41, |v18|, |v19|, |v20|
	v_max3_f32 v42, |v21|, |v22|, |v23|
	v_max3_f32 v43, |v24|, |v25|, |v26|
	v_max3_f32 v44, |v27|, |v28|, |v29|
	v_max3_f32 v45, |v30|, |v31|, |v32|
	v_max3_f32 v41, v41, v42, |v33|
	v_max3_f32 v43, v43, v44, v45
	v_max_f32_e32 v41, v41, v43
	v_pk_add_f32 v[2:3], v[2:3], v[18:19]
	v_pk_add_f32 v[4:5], v[4:5], v[20:21]
	v_max_f32_dpp v41, v41, v41 quad_perm:[1,0,3,2] row_mask:0xf bank_mask:0xf
	v_pk_add_f32 v[6:7], v[6:7], v[22:23]
	v_pk_add_f32 v[8:9], v[8:9], v[24:25]
	v_max_f32_dpp v41, v41, v41 quad_perm:[2,3,0,1] row_mask:0xf bank_mask:0xf
	v_pk_add_f32 v[10:11], v[10:11], v[26:27]
	v_pk_add_f32 v[12:13], v[12:13], v[28:29]
	v_max_f32_dpp v41, v41, v41 row_half_mirror row_mask:0xf bank_mask:0xf
	v_pk_add_f32 v[14:15], v[14:15], v[30:31]
	v_pk_add_f32 v[16:17], v[16:17], v[32:33]
	v_max_f32_dpp v41, v41, v41 row_mirror row_mask:0xf bank_mask:0xf
	s_nop 1
	v_max_f32_dpp v41, v41, v41 row_bcast:15 row_mask:0xa bank_mask:0xf
	s_nop 1
	v_max_f32_dpp v41, v41, v41 row_bcast:31 row_mask:0xc bank_mask:0xf
	s_nop 1
	v_readlane_b32 s28, v41, 63
	s_nop 1
	v_div_scale_f32 v48, s[30:31], s28, s28, v47
	v_rcp_f32_e32 v49, v48
	s_nop 0
	v_fma_f32 v50, -v48, v49, 1.0
	v_fmac_f32_e32 v49, v50, v49
	v_mov_b32_e32 v50, s28
	v_div_scale_f32 v50, vcc, s32, v50, s32
	v_mul_f32_e32 v51, v50, v49
	v_fma_f32 v52, -v48, v51, v50
	v_fmac_f32_e32 v51, v52, v49
	v_fma_f32 v48, -v48, v51, v50
	v_div_fmas_f32 v48, v48, v49, v51
	v_div_fixup_f32 v48, v48, s28, v47
	v_cmp_gt_f32_e64 vcc, s28, 0
	v_writelane_b32 v40, s28, 10
	s_nop 0
	v_cndmask_b32_e32 v48, 0, v48, vcc
	v_fmaak_f32 v49, v18, v48, 0x4b400000
	v_fmaak_f32 v50, v19, v48, 0x4b400000
	v_fmaak_f32 v51, v20, v48, 0x4b400000
	v_fmaak_f32 v52, v21, v48, 0x4b400000
	v_perm_b32 v49, v50, v49, s33
	v_perm_b32 v51, v52, v51, s34
	v_or_b32_e32 v96, v49, v51
	v_fmaak_f32 v53, v22, v48, 0x4b400000
	v_fmaak_f32 v54, v23, v48, 0x4b400000
	v_fmaak_f32 v55, v24, v48, 0x4b400000
	v_fmaak_f32 v46, v25, v48, 0x4b400000
	v_perm_b32 v53, v54, v53, s33
	v_perm_b32 v55, v46, v55, s34
	v_or_b32_e32 v97, v53, v55
	v_fmaak_f32 v49, v26, v48, 0x4b400000
	v_fmaak_f32 v50, v27, v48, 0x4b400000
	v_fmaak_f32 v51, v28, v48, 0x4b400000
	v_fmaak_f32 v52, v29, v48, 0x4b400000
	v_perm_b32 v49, v50, v49, s33
	v_perm_b32 v51, v52, v51, s34
	v_or_b32_e32 v98, v49, v51
	v_fmaak_f32 v53, v30, v48, 0x4b400000
	v_fmaak_f32 v54, v31, v48, 0x4b400000
	v_fmaak_f32 v55, v32, v48, 0x4b400000
	v_fmaak_f32 v46, v33, v48, 0x4b400000
	v_perm_b32 v53, v54, v53, s33
	v_perm_b32 v55, v46, v55, s34
	v_or_b32_e32 v99, v53, v55
	s_waitcnt vmcnt(0)
	ds_read_b128 v[18:21], v38 offset:0
	ds_read_b128 v[22:25], v38 offset:1024
	ds_read_b128 v[26:29], v38 offset:2048
	ds_read_b128 v[30:33], v38 offset:3072
	s_waitcnt lgkmcnt(0)
	s_mov_b32 m0, s35
	s_nop 0
	global_load_lds_dwordx4 v34, s[16:17] nt
	global_load_lds_dwordx4 v34, s[16:17] offset:1024 nt
	global_load_lds_dwordx4 v34, s[16:17] offset:2048 nt
	global_load_lds_dwordx4 v35, s[16:17] offset:3072 nt
	s_add_u32 s16, s16, 0x7d00
	s_addc_u32 s17, s17, 0
	v_cndmask_b32_e64 v30, 0, v30, s[18:19]
	v_cndmask_b32_e64 v31, 0, v31, s[18:19]
	v_cndmask_b32_e64 v32, 0, v32, s[18:19]
	v_cndmask_b32_e64 v33, 0, v33, s[18:19]
	v_max3_f32 v41, |v18|, |v19|, |v20|
	v_max3_f32 v42, |v21|, |v22|, |v23|
	v_max3_f32 v43, |v24|, |v25|, |v26|
	v_max3_f32 v44, |v27|, |v28|, |v29|
	v_max3_f32 v45, |v30|, |v31|, |v32|
	v_max3_f32 v41, v41, v42, |v33|
	v_max3_f32 v43, v43, v44, v45
	v_max_f32_e32 v41, v41, v43
	v_pk_add_f32 v[2:3], v[2:3], v[18:19]
	v_pk_add_f32 v[4:5], v[4:5], v[20:21]
	v_max_f32_dpp v41, v41, v41 quad_perm:[1,0,3,2] row_mask:0xf bank_mask:0xf
	v_pk_add_f32 v[6:7], v[6:7], v[22:23]
	v_pk_add_f32 v[8:9], v[8:9], v[24:25]
	v_max_f32_dpp v41, v41, v41 quad_perm:[2,3,0,1] row_mask:0xf bank_mask:0xf
	v_pk_add_f32 v[10:11], v[10:11], v[26:27]
	v_pk_add_f32 v[12:13], v[12:13], v[28:29]
	v_max_f32_dpp v41, v41, v41 row_half_mirror row_mask:0xf bank_mask:0xf
	v_pk_add_f32 v[14:15], v[14:15], v[30:31]
	v_pk_add_f32 v[16:17], v[16:17], v[32:33]
	v_max_f32_dpp v41, v41, v41 row_mirror row_mask:0xf bank_mask:0xf
	s_nop 1
	v_max_f32_dpp v41, v41, v41 row_bcast:15 row_mask:0xa bank_mask:0xf
	s_nop 1
	v_max_f32_dpp v41, v41, v41 row_bcast:31 row_mask:0xc bank_mask:0xf
	s_nop 1
	v_readlane_b32 s28, v41, 63
	s_nop 1
	v_div_scale_f32 v48, s[30:31], s28, s28, v47
	v_rcp_f32_e32 v49, v48
	s_nop 0
	v_fma_f32 v50, -v48, v49, 1.0
	v_fmac_f32_e32 v49, v50, v49
	v_mov_b32_e32 v50, s28
	v_div_scale_f32 v50, vcc, s32, v50, s32
	v_mul_f32_e32 v51, v50, v49
	v_fma_f32 v52, -v48, v51, v50
	v_fmac_f32_e32 v51, v52, v49
	v_fma_f32 v48, -v48, v51, v50
	v_div_fmas_f32 v48, v48, v49, v51
	v_div_fixup_f32 v48, v48, s28, v47
	v_cmp_gt_f32_e64 vcc, s28, 0
	v_writelane_b32 v40, s28, 11
	s_nop 0
	v_cndmask_b32_e32 v48, 0, v48, vcc
	v_fmaak_f32 v49, v18, v48, 0x4b400000
	v_fmaak_f32 v50, v19, v48, 0x4b400000
	v_fmaak_f32 v51, v20, v48, 0x4b400000
	v_fmaak_f32 v52, v21, v48, 0x4b400000
	v_perm_b32 v49, v50, v49, s33
	v_perm_b32 v51, v52, v51, s34
	v_or_b32_e32 v100, v49, v51
	v_fmaak_f32 v53, v22, v48, 0x4b400000
	v_fmaak_f32 v54, v23, v48, 0x4b400000
	v_fmaak_f32 v55, v24, v48, 0x4b400000
	v_fmaak_f32 v46, v25, v48, 0x4b400000
	v_perm_b32 v53, v54, v53, s33
	v_perm_b32 v55, v46, v55, s34
	v_or_b32_e32 v101, v53, v55
	v_fmaak_f32 v49, v26, v48, 0x4b400000
	v_fmaak_f32 v50, v27, v48, 0x4b400000
	v_fmaak_f32 v51, v28, v48, 0x4b400000
	v_fmaak_f32 v52, v29, v48, 0x4b400000
	v_perm_b32 v49, v50, v49, s33
	v_perm_b32 v51, v52, v51, s34
	v_or_b32_e32 v102, v49, v51
	v_fmaak_f32 v53, v30, v48, 0x4b400000
	v_fmaak_f32 v54, v31, v48, 0x4b400000
	v_fmaak_f32 v55, v32, v48, 0x4b400000
	v_fmaak_f32 v46, v33, v48, 0x4b400000
	v_perm_b32 v53, v54, v53, s33
	v_perm_b32 v55, v46, v55, s34
	v_or_b32_e32 v103, v53, v55
	s_waitcnt vmcnt(0)
	ds_read_b128 v[18:21], v38 offset:0
	ds_read_b128 v[22:25], v38 offset:1024
	ds_read_b128 v[26:29], v38 offset:2048
	ds_read_b128 v[30:33], v38 offset:3072
	s_waitcnt lgkmcnt(0)
	s_mov_b32 m0, s35
	s_nop 0
	global_load_lds_dwordx4 v34, s[16:17] nt
	global_load_lds_dwordx4 v34, s[16:17] offset:1024 nt
	global_load_lds_dwordx4 v34, s[16:17] offset:2048 nt
	global_load_lds_dwordx4 v35, s[16:17] offset:3072 nt
	s_add_u32 s16, s16, 0x7d00
	s_addc_u32 s17, s17, 0
	v_cndmask_b32_e64 v30, 0, v30, s[18:19]
	v_cndmask_b32_e64 v31, 0, v31, s[18:19]
	v_cndmask_b32_e64 v32, 0, v32, s[18:19]
	v_cndmask_b32_e64 v33, 0, v33, s[18:19]
	v_max3_f32 v41, |v18|, |v19|, |v20|
	v_max3_f32 v42, |v21|, |v22|, |v23|
	v_max3_f32 v43, |v24|, |v25|, |v26|
	v_max3_f32 v44, |v27|, |v28|, |v29|
	v_max3_f32 v45, |v30|, |v31|, |v32|
	v_max3_f32 v41, v41, v42, |v33|
	v_max3_f32 v43, v43, v44, v45
	v_max_f32_e32 v41, v41, v43
	v_pk_add_f32 v[2:3], v[2:3], v[18:19]
	v_pk_add_f32 v[4:5], v[4:5], v[20:21]
	v_max_f32_dpp v41, v41, v41 quad_perm:[1,0,3,2] row_mask:0xf bank_mask:0xf
	v_pk_add_f32 v[6:7], v[6:7], v[22:23]
	v_pk_add_f32 v[8:9], v[8:9], v[24:25]
	v_max_f32_dpp v41, v41, v41 quad_perm:[2,3,0,1] row_mask:0xf bank_mask:0xf
	v_pk_add_f32 v[10:11], v[10:11], v[26:27]
	v_pk_add_f32 v[12:13], v[12:13], v[28:29]
	v_max_f32_dpp v41, v41, v41 row_half_mirror row_mask:0xf bank_mask:0xf
	v_pk_add_f32 v[14:15], v[14:15], v[30:31]
	v_pk_add_f32 v[16:17], v[16:17], v[32:33]
	v_max_f32_dpp v41, v41, v41 row_mirror row_mask:0xf bank_mask:0xf
	s_nop 1
	v_max_f32_dpp v41, v41, v41 row_bcast:15 row_mask:0xa bank_mask:0xf
	s_nop 1
	v_max_f32_dpp v41, v41, v41 row_bcast:31 row_mask:0xc bank_mask:0xf
	s_nop 1
	v_readlane_b32 s28, v41, 63
	s_nop 1
	v_div_scale_f32 v48, s[30:31], s28, s28, v47
	v_rcp_f32_e32 v49, v48
	s_nop 0
	v_fma_f32 v50, -v48, v49, 1.0
	v_fmac_f32_e32 v49, v50, v49
	v_mov_b32_e32 v50, s28
	v_div_scale_f32 v50, vcc, s32, v50, s32
	v_mul_f32_e32 v51, v50, v49
	v_fma_f32 v52, -v48, v51, v50
	v_fmac_f32_e32 v51, v52, v49
	v_fma_f32 v48, -v48, v51, v50
	v_div_fmas_f32 v48, v48, v49, v51
	v_div_fixup_f32 v48, v48, s28, v47
	v_cmp_gt_f32_e64 vcc, s28, 0
	v_writelane_b32 v40, s28, 12
	s_nop 0
	v_cndmask_b32_e32 v48, 0, v48, vcc
	v_fmaak_f32 v49, v18, v48, 0x4b400000
	v_fmaak_f32 v50, v19, v48, 0x4b400000
	v_fmaak_f32 v51, v20, v48, 0x4b400000
	v_fmaak_f32 v52, v21, v48, 0x4b400000
	v_perm_b32 v49, v50, v49, s33
	v_perm_b32 v51, v52, v51, s34
	v_or_b32_e32 v104, v49, v51
	v_fmaak_f32 v53, v22, v48, 0x4b400000
	v_fmaak_f32 v54, v23, v48, 0x4b400000
	v_fmaak_f32 v55, v24, v48, 0x4b400000
	v_fmaak_f32 v46, v25, v48, 0x4b400000
	v_perm_b32 v53, v54, v53, s33
	v_perm_b32 v55, v46, v55, s34
	v_or_b32_e32 v105, v53, v55
	v_fmaak_f32 v49, v26, v48, 0x4b400000
	v_fmaak_f32 v50, v27, v48, 0x4b400000
	v_fmaak_f32 v51, v28, v48, 0x4b400000
	v_fmaak_f32 v52, v29, v48, 0x4b400000
	v_perm_b32 v49, v50, v49, s33
	v_perm_b32 v51, v52, v51, s34
	v_or_b32_e32 v106, v49, v51
	v_fmaak_f32 v53, v30, v48, 0x4b400000
	v_fmaak_f32 v54, v31, v48, 0x4b400000
	v_fmaak_f32 v55, v32, v48, 0x4b400000
	v_fmaak_f32 v46, v33, v48, 0x4b400000
	v_perm_b32 v53, v54, v53, s33
	v_perm_b32 v55, v46, v55, s34
	v_or_b32_e32 v107, v53, v55
	s_waitcnt vmcnt(0)
	ds_read_b128 v[18:21], v38 offset:0
	ds_read_b128 v[22:25], v38 offset:1024
	ds_read_b128 v[26:29], v38 offset:2048
	ds_read_b128 v[30:33], v38 offset:3072
	s_waitcnt lgkmcnt(0)
	s_mov_b32 m0, s35
	s_nop 0
	global_load_lds_dwordx4 v34, s[16:17] nt
	global_load_lds_dwordx4 v34, s[16:17] offset:1024 nt
	global_load_lds_dwordx4 v34, s[16:17] offset:2048 nt
	global_load_lds_dwordx4 v35, s[16:17] offset:3072 nt
	s_add_u32 s16, s16, 0x7d00
	s_addc_u32 s17, s17, 0
	v_cndmask_b32_e64 v30, 0, v30, s[18:19]
	v_cndmask_b32_e64 v31, 0, v31, s[18:19]
	v_cndmask_b32_e64 v32, 0, v32, s[18:19]
	v_cndmask_b32_e64 v33, 0, v33, s[18:19]
	v_max3_f32 v41, |v18|, |v19|, |v20|
	v_max3_f32 v42, |v21|, |v22|, |v23|
	v_max3_f32 v43, |v24|, |v25|, |v26|
	v_max3_f32 v44, |v27|, |v28|, |v29|
	v_max3_f32 v45, |v30|, |v31|, |v32|
	v_max3_f32 v41, v41, v42, |v33|
	v_max3_f32 v43, v43, v44, v45
	v_max_f32_e32 v41, v41, v43
	v_pk_add_f32 v[2:3], v[2:3], v[18:19]
	v_pk_add_f32 v[4:5], v[4:5], v[20:21]
	v_max_f32_dpp v41, v41, v41 quad_perm:[1,0,3,2] row_mask:0xf bank_mask:0xf
	v_pk_add_f32 v[6:7], v[6:7], v[22:23]
	v_pk_add_f32 v[8:9], v[8:9], v[24:25]
	v_max_f32_dpp v41, v41, v41 quad_perm:[2,3,0,1] row_mask:0xf bank_mask:0xf
	v_pk_add_f32 v[10:11], v[10:11], v[26:27]
	v_pk_add_f32 v[12:13], v[12:13], v[28:29]
	v_max_f32_dpp v41, v41, v41 row_half_mirror row_mask:0xf bank_mask:0xf
	v_pk_add_f32 v[14:15], v[14:15], v[30:31]
	v_pk_add_f32 v[16:17], v[16:17], v[32:33]
	v_max_f32_dpp v41, v41, v41 row_mirror row_mask:0xf bank_mask:0xf
	s_nop 1
	v_max_f32_dpp v41, v41, v41 row_bcast:15 row_mask:0xa bank_mask:0xf
	s_nop 1
	v_max_f32_dpp v41, v41, v41 row_bcast:31 row_mask:0xc bank_mask:0xf
	s_nop 1
	v_readlane_b32 s28, v41, 63
	s_nop 1
	v_div_scale_f32 v48, s[30:31], s28, s28, v47
	v_rcp_f32_e32 v49, v48
	s_nop 0
	v_fma_f32 v50, -v48, v49, 1.0
	v_fmac_f32_e32 v49, v50, v49
	v_mov_b32_e32 v50, s28
	v_div_scale_f32 v50, vcc, s32, v50, s32
	v_mul_f32_e32 v51, v50, v49
	v_fma_f32 v52, -v48, v51, v50
	v_fmac_f32_e32 v51, v52, v49
	v_fma_f32 v48, -v48, v51, v50
	v_div_fmas_f32 v48, v48, v49, v51
	v_div_fixup_f32 v48, v48, s28, v47
	v_cmp_gt_f32_e64 vcc, s28, 0
	v_writelane_b32 v40, s28, 13
	s_nop 0
	v_cndmask_b32_e32 v48, 0, v48, vcc
	v_fmaak_f32 v49, v18, v48, 0x4b400000
	v_fmaak_f32 v50, v19, v48, 0x4b400000
	v_fmaak_f32 v51, v20, v48, 0x4b400000
	v_fmaak_f32 v52, v21, v48, 0x4b400000
	v_perm_b32 v49, v50, v49, s33
	v_perm_b32 v51, v52, v51, s34
	v_or_b32_e32 v108, v49, v51
	v_fmaak_f32 v53, v22, v48, 0x4b400000
	v_fmaak_f32 v54, v23, v48, 0x4b400000
	v_fmaak_f32 v55, v24, v48, 0x4b400000
	v_fmaak_f32 v46, v25, v48, 0x4b400000
	v_perm_b32 v53, v54, v53, s33
	v_perm_b32 v55, v46, v55, s34
	v_or_b32_e32 v109, v53, v55
	v_fmaak_f32 v49, v26, v48, 0x4b400000
	v_fmaak_f32 v50, v27, v48, 0x4b400000
	v_fmaak_f32 v51, v28, v48, 0x4b400000
	v_fmaak_f32 v52, v29, v48, 0x4b400000
	v_perm_b32 v49, v50, v49, s33
	v_perm_b32 v51, v52, v51, s34
	v_or_b32_e32 v110, v49, v51
	v_fmaak_f32 v53, v30, v48, 0x4b400000
	v_fmaak_f32 v54, v31, v48, 0x4b400000
	v_fmaak_f32 v55, v32, v48, 0x4b400000
	v_fmaak_f32 v46, v33, v48, 0x4b400000
	v_perm_b32 v53, v54, v53, s33
	v_perm_b32 v55, v46, v55, s34
	v_or_b32_e32 v111, v53, v55
	s_waitcnt vmcnt(0)
	ds_read_b128 v[18:21], v38 offset:0
	ds_read_b128 v[22:25], v38 offset:1024
	ds_read_b128 v[26:29], v38 offset:2048
	ds_read_b128 v[30:33], v38 offset:3072
	s_waitcnt lgkmcnt(0)
	s_mov_b32 m0, s35
	s_nop 0
	global_load_lds_dwordx4 v34, s[16:17] nt
	global_load_lds_dwordx4 v34, s[16:17] offset:1024 nt
	global_load_lds_dwordx4 v34, s[16:17] offset:2048 nt
	global_load_lds_dwordx4 v35, s[16:17] offset:3072 nt
	s_add_u32 s16, s16, 0x7d00
	s_addc_u32 s17, s17, 0
	v_cndmask_b32_e64 v30, 0, v30, s[18:19]
	v_cndmask_b32_e64 v31, 0, v31, s[18:19]
	v_cndmask_b32_e64 v32, 0, v32, s[18:19]
	v_cndmask_b32_e64 v33, 0, v33, s[18:19]
	v_max3_f32 v41, |v18|, |v19|, |v20|
	v_max3_f32 v42, |v21|, |v22|, |v23|
	v_max3_f32 v43, |v24|, |v25|, |v26|
	v_max3_f32 v44, |v27|, |v28|, |v29|
	v_max3_f32 v45, |v30|, |v31|, |v32|
	v_max3_f32 v41, v41, v42, |v33|
	v_max3_f32 v43, v43, v44, v45
	v_max_f32_e32 v41, v41, v43
	v_pk_add_f32 v[2:3], v[2:3], v[18:19]
	v_pk_add_f32 v[4:5], v[4:5], v[20:21]
	v_max_f32_dpp v41, v41, v41 quad_perm:[1,0,3,2] row_mask:0xf bank_mask:0xf
	v_pk_add_f32 v[6:7], v[6:7], v[22:23]
	v_pk_add_f32 v[8:9], v[8:9], v[24:25]
	v_max_f32_dpp v41, v41, v41 quad_perm:[2,3,0,1] row_mask:0xf bank_mask:0xf
	v_pk_add_f32 v[10:11], v[10:11], v[26:27]
	v_pk_add_f32 v[12:13], v[12:13], v[28:29]
	v_max_f32_dpp v41, v41, v41 row_half_mirror row_mask:0xf bank_mask:0xf
	v_pk_add_f32 v[14:15], v[14:15], v[30:31]
	v_pk_add_f32 v[16:17], v[16:17], v[32:33]
	v_max_f32_dpp v41, v41, v41 row_mirror row_mask:0xf bank_mask:0xf
	s_nop 1
	v_max_f32_dpp v41, v41, v41 row_bcast:15 row_mask:0xa bank_mask:0xf
	s_nop 1
	v_max_f32_dpp v41, v41, v41 row_bcast:31 row_mask:0xc bank_mask:0xf
	s_nop 1
	v_readlane_b32 s28, v41, 63
	s_nop 1
	v_div_scale_f32 v48, s[30:31], s28, s28, v47
	v_rcp_f32_e32 v49, v48
	s_nop 0
	v_fma_f32 v50, -v48, v49, 1.0
	v_fmac_f32_e32 v49, v50, v49
	v_mov_b32_e32 v50, s28
	v_div_scale_f32 v50, vcc, s32, v50, s32
	v_mul_f32_e32 v51, v50, v49
	v_fma_f32 v52, -v48, v51, v50
	v_fmac_f32_e32 v51, v52, v49
	v_fma_f32 v48, -v48, v51, v50
	v_div_fmas_f32 v48, v48, v49, v51
	v_div_fixup_f32 v48, v48, s28, v47
	v_cmp_gt_f32_e64 vcc, s28, 0
	v_writelane_b32 v40, s28, 14
	s_nop 0
	v_cndmask_b32_e32 v48, 0, v48, vcc
	v_fmaak_f32 v49, v18, v48, 0x4b400000
	v_fmaak_f32 v50, v19, v48, 0x4b400000
	v_fmaak_f32 v51, v20, v48, 0x4b400000
	v_fmaak_f32 v52, v21, v48, 0x4b400000
	v_perm_b32 v49, v50, v49, s33
	v_perm_b32 v51, v52, v51, s34
	v_or_b32_e32 v112, v49, v51
	v_fmaak_f32 v53, v22, v48, 0x4b400000
	v_fmaak_f32 v54, v23, v48, 0x4b400000
	v_fmaak_f32 v55, v24, v48, 0x4b400000
	v_fmaak_f32 v46, v25, v48, 0x4b400000
	v_perm_b32 v53, v54, v53, s33
	v_perm_b32 v55, v46, v55, s34
	v_or_b32_e32 v113, v53, v55
	v_fmaak_f32 v49, v26, v48, 0x4b400000
	v_fmaak_f32 v50, v27, v48, 0x4b400000
	v_fmaak_f32 v51, v28, v48, 0x4b400000
	v_fmaak_f32 v52, v29, v48, 0x4b400000
	v_perm_b32 v49, v50, v49, s33
	v_perm_b32 v51, v52, v51, s34
	v_or_b32_e32 v114, v49, v51
	v_fmaak_f32 v53, v30, v48, 0x4b400000
	v_fmaak_f32 v54, v31, v48, 0x4b400000
	v_fmaak_f32 v55, v32, v48, 0x4b400000
	v_fmaak_f32 v46, v33, v48, 0x4b400000
	v_perm_b32 v53, v54, v53, s33
	v_perm_b32 v55, v46, v55, s34
	v_or_b32_e32 v115, v53, v55
	s_waitcnt vmcnt(0)
	ds_read_b128 v[18:21], v38 offset:0
	ds_read_b128 v[22:25], v38 offset:1024
	ds_read_b128 v[26:29], v38 offset:2048
	ds_read_b128 v[30:33], v38 offset:3072
	s_waitcnt lgkmcnt(0)
	s_mov_b32 m0, s35
	s_nop 0
	global_load_lds_dwordx4 v34, s[16:17] nt
	global_load_lds_dwordx4 v34, s[16:17] offset:1024 nt
	global_load_lds_dwordx4 v34, s[16:17] offset:2048 nt
	global_load_lds_dwordx4 v35, s[16:17] offset:3072 nt
	s_add_u32 s16, s16, 0x7d00
	s_addc_u32 s17, s17, 0
	v_cndmask_b32_e64 v30, 0, v30, s[18:19]
	v_cndmask_b32_e64 v31, 0, v31, s[18:19]
	v_cndmask_b32_e64 v32, 0, v32, s[18:19]
	v_cndmask_b32_e64 v33, 0, v33, s[18:19]
	v_max3_f32 v41, |v18|, |v19|, |v20|
	v_max3_f32 v42, |v21|, |v22|, |v23|
	v_max3_f32 v43, |v24|, |v25|, |v26|
	v_max3_f32 v44, |v27|, |v28|, |v29|
	v_max3_f32 v45, |v30|, |v31|, |v32|
	v_max3_f32 v41, v41, v42, |v33|
	v_max3_f32 v43, v43, v44, v45
	v_max_f32_e32 v41, v41, v43
	v_pk_add_f32 v[2:3], v[2:3], v[18:19]
	v_pk_add_f32 v[4:5], v[4:5], v[20:21]
	v_max_f32_dpp v41, v41, v41 quad_perm:[1,0,3,2] row_mask:0xf bank_mask:0xf
	v_pk_add_f32 v[6:7], v[6:7], v[22:23]
	v_pk_add_f32 v[8:9], v[8:9], v[24:25]
	v_max_f32_dpp v41, v41, v41 quad_perm:[2,3,0,1] row_mask:0xf bank_mask:0xf
	v_pk_add_f32 v[10:11], v[10:11], v[26:27]
	v_pk_add_f32 v[12:13], v[12:13], v[28:29]
	v_max_f32_dpp v41, v41, v41 row_half_mirror row_mask:0xf bank_mask:0xf
	v_pk_add_f32 v[14:15], v[14:15], v[30:31]
	v_pk_add_f32 v[16:17], v[16:17], v[32:33]
	v_max_f32_dpp v41, v41, v41 row_mirror row_mask:0xf bank_mask:0xf
	s_nop 1
	v_max_f32_dpp v41, v41, v41 row_bcast:15 row_mask:0xa bank_mask:0xf
	s_nop 1
	v_max_f32_dpp v41, v41, v41 row_bcast:31 row_mask:0xc bank_mask:0xf
	s_nop 1
	v_readlane_b32 s28, v41, 63
	s_nop 1
	v_div_scale_f32 v48, s[30:31], s28, s28, v47
	v_rcp_f32_e32 v49, v48
	s_nop 0
	v_fma_f32 v50, -v48, v49, 1.0
	v_fmac_f32_e32 v49, v50, v49
	v_mov_b32_e32 v50, s28
	v_div_scale_f32 v50, vcc, s32, v50, s32
	v_mul_f32_e32 v51, v50, v49
	v_fma_f32 v52, -v48, v51, v50
	v_fmac_f32_e32 v51, v52, v49
	v_fma_f32 v48, -v48, v51, v50
	v_div_fmas_f32 v48, v48, v49, v51
	v_div_fixup_f32 v48, v48, s28, v47
	v_cmp_gt_f32_e64 vcc, s28, 0
	v_writelane_b32 v40, s28, 15
	s_nop 0
	v_cndmask_b32_e32 v48, 0, v48, vcc
	v_fmaak_f32 v49, v18, v48, 0x4b400000
	v_fmaak_f32 v50, v19, v48, 0x4b400000
	v_fmaak_f32 v51, v20, v48, 0x4b400000
	v_fmaak_f32 v52, v21, v48, 0x4b400000
	v_perm_b32 v49, v50, v49, s33
	v_perm_b32 v51, v52, v51, s34
	v_or_b32_e32 v116, v49, v51
	v_fmaak_f32 v53, v22, v48, 0x4b400000
	v_fmaak_f32 v54, v23, v48, 0x4b400000
	v_fmaak_f32 v55, v24, v48, 0x4b400000
	v_fmaak_f32 v46, v25, v48, 0x4b400000
	v_perm_b32 v53, v54, v53, s33
	v_perm_b32 v55, v46, v55, s34
	v_or_b32_e32 v117, v53, v55
	v_fmaak_f32 v49, v26, v48, 0x4b400000
	v_fmaak_f32 v50, v27, v48, 0x4b400000
	v_fmaak_f32 v51, v28, v48, 0x4b400000
	v_fmaak_f32 v52, v29, v48, 0x4b400000
	v_perm_b32 v49, v50, v49, s33
	v_perm_b32 v51, v52, v51, s34
	v_or_b32_e32 v118, v49, v51
	v_fmaak_f32 v53, v30, v48, 0x4b400000
	v_fmaak_f32 v54, v31, v48, 0x4b400000
	v_fmaak_f32 v55, v32, v48, 0x4b400000
	v_fmaak_f32 v46, v33, v48, 0x4b400000
	v_perm_b32 v53, v54, v53, s33
	v_perm_b32 v55, v46, v55, s34
	v_or_b32_e32 v119, v53, v55
	s_waitcnt vmcnt(0)
	ds_read_b128 v[18:21], v38 offset:0
	ds_read_b128 v[22:25], v38 offset:1024
	ds_read_b128 v[26:29], v38 offset:2048
	ds_read_b128 v[30:33], v38 offset:3072
	s_waitcnt lgkmcnt(0)
	s_mov_b32 m0, s35
	s_nop 0
	global_load_lds_dwordx4 v34, s[16:17] nt
	global_load_lds_dwordx4 v34, s[16:17] offset:1024 nt
	global_load_lds_dwordx4 v34, s[16:17] offset:2048 nt
	global_load_lds_dwordx4 v35, s[16:17] offset:3072 nt
	s_add_u32 s16, s16, 0x7d00
	s_addc_u32 s17, s17, 0
	v_cndmask_b32_e64 v30, 0, v30, s[18:19]
	v_cndmask_b32_e64 v31, 0, v31, s[18:19]
	v_cndmask_b32_e64 v32, 0, v32, s[18:19]
	v_cndmask_b32_e64 v33, 0, v33, s[18:19]
	v_max3_f32 v41, |v18|, |v19|, |v20|
	v_max3_f32 v42, |v21|, |v22|, |v23|
	v_max3_f32 v43, |v24|, |v25|, |v26|
	v_max3_f32 v44, |v27|, |v28|, |v29|
	v_max3_f32 v45, |v30|, |v31|, |v32|
	v_max3_f32 v41, v41, v42, |v33|
	v_max3_f32 v43, v43, v44, v45
	v_max_f32_e32 v41, v41, v43
	v_pk_add_f32 v[2:3], v[2:3], v[18:19]
	v_pk_add_f32 v[4:5], v[4:5], v[20:21]
	v_max_f32_dpp v41, v41, v41 quad_perm:[1,0,3,2] row_mask:0xf bank_mask:0xf
	v_pk_add_f32 v[6:7], v[6:7], v[22:23]
	v_pk_add_f32 v[8:9], v[8:9], v[24:25]
	v_max_f32_dpp v41, v41, v41 quad_perm:[2,3,0,1] row_mask:0xf bank_mask:0xf
	v_pk_add_f32 v[10:11], v[10:11], v[26:27]
	v_pk_add_f32 v[12:13], v[12:13], v[28:29]
	v_max_f32_dpp v41, v41, v41 row_half_mirror row_mask:0xf bank_mask:0xf
	v_pk_add_f32 v[14:15], v[14:15], v[30:31]
	v_pk_add_f32 v[16:17], v[16:17], v[32:33]
	v_max_f32_dpp v41, v41, v41 row_mirror row_mask:0xf bank_mask:0xf
	s_nop 1
	v_max_f32_dpp v41, v41, v41 row_bcast:15 row_mask:0xa bank_mask:0xf
	s_nop 1
	v_max_f32_dpp v41, v41, v41 row_bcast:31 row_mask:0xc bank_mask:0xf
	s_nop 1
	v_readlane_b32 s28, v41, 63
	s_nop 1
	v_div_scale_f32 v48, s[30:31], s28, s28, v47
	v_rcp_f32_e32 v49, v48
	s_nop 0
	v_fma_f32 v50, -v48, v49, 1.0
	v_fmac_f32_e32 v49, v50, v49
	v_mov_b32_e32 v50, s28
	v_div_scale_f32 v50, vcc, s32, v50, s32
	v_mul_f32_e32 v51, v50, v49
	v_fma_f32 v52, -v48, v51, v50
	v_fmac_f32_e32 v51, v52, v49
	v_fma_f32 v48, -v48, v51, v50
	v_div_fmas_f32 v48, v48, v49, v51
	v_div_fixup_f32 v48, v48, s28, v47
	v_cmp_gt_f32_e64 vcc, s28, 0
	v_writelane_b32 v40, s28, 16
	s_nop 0
	v_cndmask_b32_e32 v48, 0, v48, vcc
	v_fmaak_f32 v49, v18, v48, 0x4b400000
	v_fmaak_f32 v50, v19, v48, 0x4b400000
	v_fmaak_f32 v51, v20, v48, 0x4b400000
	v_fmaak_f32 v52, v21, v48, 0x4b400000
	v_perm_b32 v49, v50, v49, s33
	v_perm_b32 v51, v52, v51, s34
	v_or_b32_e32 v120, v49, v51
	v_fmaak_f32 v53, v22, v48, 0x4b400000
	v_fmaak_f32 v54, v23, v48, 0x4b400000
	v_fmaak_f32 v55, v24, v48, 0x4b400000
	v_fmaak_f32 v46, v25, v48, 0x4b400000
	v_perm_b32 v53, v54, v53, s33
	v_perm_b32 v55, v46, v55, s34
	v_or_b32_e32 v121, v53, v55
	v_fmaak_f32 v49, v26, v48, 0x4b400000
	v_fmaak_f32 v50, v27, v48, 0x4b400000
	v_fmaak_f32 v51, v28, v48, 0x4b400000
	v_fmaak_f32 v52, v29, v48, 0x4b400000
	v_perm_b32 v49, v50, v49, s33
	v_perm_b32 v51, v52, v51, s34
	v_or_b32_e32 v122, v49, v51
	v_fmaak_f32 v53, v30, v48, 0x4b400000
	v_fmaak_f32 v54, v31, v48, 0x4b400000
	v_fmaak_f32 v55, v32, v48, 0x4b400000
	v_fmaak_f32 v46, v33, v48, 0x4b400000
	v_perm_b32 v53, v54, v53, s33
	v_perm_b32 v55, v46, v55, s34
	v_or_b32_e32 v123, v53, v55
	s_waitcnt vmcnt(0)
	ds_read_b128 v[18:21], v38 offset:0
	ds_read_b128 v[22:25], v38 offset:1024
	ds_read_b128 v[26:29], v38 offset:2048
	ds_read_b128 v[30:33], v38 offset:3072
	s_waitcnt lgkmcnt(0)
	s_mov_b32 m0, s35
	s_nop 0
	global_load_lds_dwordx4 v34, s[16:17] nt
	global_load_lds_dwordx4 v34, s[16:17] offset:1024 nt
	global_load_lds_dwordx4 v34, s[16:17] offset:2048 nt
	global_load_lds_dwordx4 v35, s[16:17] offset:3072 nt
	s_add_u32 s16, s16, 0x7d00
	s_addc_u32 s17, s17, 0
	v_cndmask_b32_e64 v30, 0, v30, s[18:19]
	v_cndmask_b32_e64 v31, 0, v31, s[18:19]
	v_cndmask_b32_e64 v32, 0, v32, s[18:19]
	v_cndmask_b32_e64 v33, 0, v33, s[18:19]
	v_max3_f32 v41, |v18|, |v19|, |v20|
	v_max3_f32 v42, |v21|, |v22|, |v23|
	v_max3_f32 v43, |v24|, |v25|, |v26|
	v_max3_f32 v44, |v27|, |v28|, |v29|
	v_max3_f32 v45, |v30|, |v31|, |v32|
	v_max3_f32 v41, v41, v42, |v33|
	v_max3_f32 v43, v43, v44, v45
	v_max_f32_e32 v41, v41, v43
	v_pk_add_f32 v[2:3], v[2:3], v[18:19]
	v_pk_add_f32 v[4:5], v[4:5], v[20:21]
	v_max_f32_dpp v41, v41, v41 quad_perm:[1,0,3,2] row_mask:0xf bank_mask:0xf
	v_pk_add_f32 v[6:7], v[6:7], v[22:23]
	v_pk_add_f32 v[8:9], v[8:9], v[24:25]
	v_max_f32_dpp v41, v41, v41 quad_perm:[2,3,0,1] row_mask:0xf bank_mask:0xf
	v_pk_add_f32 v[10:11], v[10:11], v[26:27]
	v_pk_add_f32 v[12:13], v[12:13], v[28:29]
	v_max_f32_dpp v41, v41, v41 row_half_mirror row_mask:0xf bank_mask:0xf
	v_pk_add_f32 v[14:15], v[14:15], v[30:31]
	v_pk_add_f32 v[16:17], v[16:17], v[32:33]
	v_max_f32_dpp v41, v41, v41 row_mirror row_mask:0xf bank_mask:0xf
	s_nop 1
	v_max_f32_dpp v41, v41, v41 row_bcast:15 row_mask:0xa bank_mask:0xf
	s_nop 1
	v_max_f32_dpp v41, v41, v41 row_bcast:31 row_mask:0xc bank_mask:0xf
	s_nop 1
	v_readlane_b32 s28, v41, 63
	s_nop 1
	v_div_scale_f32 v48, s[30:31], s28, s28, v47
	v_rcp_f32_e32 v49, v48
	s_nop 0
	v_fma_f32 v50, -v48, v49, 1.0
	v_fmac_f32_e32 v49, v50, v49
	v_mov_b32_e32 v50, s28
	v_div_scale_f32 v50, vcc, s32, v50, s32
	v_mul_f32_e32 v51, v50, v49
	v_fma_f32 v52, -v48, v51, v50
	v_fmac_f32_e32 v51, v52, v49
	v_fma_f32 v48, -v48, v51, v50
	v_div_fmas_f32 v48, v48, v49, v51
	v_div_fixup_f32 v48, v48, s28, v47
	v_cmp_gt_f32_e64 vcc, s28, 0
	v_writelane_b32 v40, s28, 17
	s_nop 0
	v_cndmask_b32_e32 v48, 0, v48, vcc
	v_fmaak_f32 v49, v18, v48, 0x4b400000
	v_fmaak_f32 v50, v19, v48, 0x4b400000
	v_fmaak_f32 v51, v20, v48, 0x4b400000
	v_fmaak_f32 v52, v21, v48, 0x4b400000
	v_perm_b32 v49, v50, v49, s33
	v_perm_b32 v51, v52, v51, s34
	v_or_b32_e32 v124, v49, v51
	v_fmaak_f32 v53, v22, v48, 0x4b400000
	v_fmaak_f32 v54, v23, v48, 0x4b400000
	v_fmaak_f32 v55, v24, v48, 0x4b400000
	v_fmaak_f32 v46, v25, v48, 0x4b400000
	v_perm_b32 v53, v54, v53, s33
	v_perm_b32 v55, v46, v55, s34
	v_or_b32_e32 v125, v53, v55
	v_fmaak_f32 v49, v26, v48, 0x4b400000
	v_fmaak_f32 v50, v27, v48, 0x4b400000
	v_fmaak_f32 v51, v28, v48, 0x4b400000
	v_fmaak_f32 v52, v29, v48, 0x4b400000
	v_perm_b32 v49, v50, v49, s33
	v_perm_b32 v51, v52, v51, s34
	v_or_b32_e32 v126, v49, v51
	v_fmaak_f32 v53, v30, v48, 0x4b400000
	v_fmaak_f32 v54, v31, v48, 0x4b400000
	v_fmaak_f32 v55, v32, v48, 0x4b400000
	v_fmaak_f32 v46, v33, v48, 0x4b400000
	v_perm_b32 v53, v54, v53, s33
	v_perm_b32 v55, v46, v55, s34
	v_or_b32_e32 v127, v53, v55
	ds_write_b128 v38, v[124:127] offset:4096
	s_waitcnt vmcnt(0)
	ds_read_b128 v[18:21], v38 offset:0
	ds_read_b128 v[22:25], v38 offset:1024
	ds_read_b128 v[26:29], v38 offset:2048
	ds_read_b128 v[30:33], v38 offset:3072
	s_waitcnt lgkmcnt(0)
	s_mov_b32 m0, s35
	s_nop 0
	global_load_lds_dwordx4 v34, s[16:17] nt
	global_load_lds_dwordx4 v34, s[16:17] offset:1024 nt
	global_load_lds_dwordx4 v34, s[16:17] offset:2048 nt
	global_load_lds_dwordx4 v35, s[16:17] offset:3072 nt
	s_add_u32 s16, s16, 0x7d00
	s_addc_u32 s17, s17, 0
	v_cndmask_b32_e64 v30, 0, v30, s[18:19]
	v_cndmask_b32_e64 v31, 0, v31, s[18:19]
	v_cndmask_b32_e64 v32, 0, v32, s[18:19]
	v_cndmask_b32_e64 v33, 0, v33, s[18:19]
	v_max3_f32 v41, |v18|, |v19|, |v20|
	v_max3_f32 v42, |v21|, |v22|, |v23|
	v_max3_f32 v43, |v24|, |v25|, |v26|
	v_max3_f32 v44, |v27|, |v28|, |v29|
	v_max3_f32 v45, |v30|, |v31|, |v32|
	v_max3_f32 v41, v41, v42, |v33|
	v_max3_f32 v43, v43, v44, v45
	v_max_f32_e32 v41, v41, v43
	v_pk_add_f32 v[2:3], v[2:3], v[18:19]
	v_pk_add_f32 v[4:5], v[4:5], v[20:21]
	v_max_f32_dpp v41, v41, v41 quad_perm:[1,0,3,2] row_mask:0xf bank_mask:0xf
	v_pk_add_f32 v[6:7], v[6:7], v[22:23]
	v_pk_add_f32 v[8:9], v[8:9], v[24:25]
	v_max_f32_dpp v41, v41, v41 quad_perm:[2,3,0,1] row_mask:0xf bank_mask:0xf
	v_pk_add_f32 v[10:11], v[10:11], v[26:27]
	v_pk_add_f32 v[12:13], v[12:13], v[28:29]
	v_max_f32_dpp v41, v41, v41 row_half_mirror row_mask:0xf bank_mask:0xf
	v_pk_add_f32 v[14:15], v[14:15], v[30:31]
	v_pk_add_f32 v[16:17], v[16:17], v[32:33]
	v_max_f32_dpp v41, v41, v41 row_mirror row_mask:0xf bank_mask:0xf
	s_nop 1
	v_max_f32_dpp v41, v41, v41 row_bcast:15 row_mask:0xa bank_mask:0xf
	s_nop 1
	v_max_f32_dpp v41, v41, v41 row_bcast:31 row_mask:0xc bank_mask:0xf
	s_nop 1
	v_readlane_b32 s28, v41, 63
	s_nop 1
	v_div_scale_f32 v48, s[30:31], s28, s28, v47
	v_rcp_f32_e32 v49, v48
	s_nop 0
	v_fma_f32 v50, -v48, v49, 1.0
	v_fmac_f32_e32 v49, v50, v49
	v_mov_b32_e32 v50, s28
	v_div_scale_f32 v50, vcc, s32, v50, s32
	v_mul_f32_e32 v51, v50, v49
	v_fma_f32 v52, -v48, v51, v50
	v_fmac_f32_e32 v51, v52, v49
	v_fma_f32 v48, -v48, v51, v50
	v_div_fmas_f32 v48, v48, v49, v51
	v_div_fixup_f32 v48, v48, s28, v47
	v_cmp_gt_f32_e64 vcc, s28, 0
	v_writelane_b32 v40, s28, 18
	s_nop 0
	v_cndmask_b32_e32 v48, 0, v48, vcc
	v_fmaak_f32 v49, v18, v48, 0x4b400000
	v_fmaak_f32 v50, v19, v48, 0x4b400000
	v_fmaak_f32 v51, v20, v48, 0x4b400000
	v_fmaak_f32 v52, v21, v48, 0x4b400000
	v_perm_b32 v49, v50, v49, s33
	v_perm_b32 v51, v52, v51, s34
	v_or_b32_e32 v124, v49, v51
	v_fmaak_f32 v53, v22, v48, 0x4b400000
	v_fmaak_f32 v54, v23, v48, 0x4b400000
	v_fmaak_f32 v55, v24, v48, 0x4b400000
	v_fmaak_f32 v46, v25, v48, 0x4b400000
	v_perm_b32 v53, v54, v53, s33
	v_perm_b32 v55, v46, v55, s34
	v_or_b32_e32 v125, v53, v55
	v_fmaak_f32 v49, v26, v48, 0x4b400000
	v_fmaak_f32 v50, v27, v48, 0x4b400000
	v_fmaak_f32 v51, v28, v48, 0x4b400000
	v_fmaak_f32 v52, v29, v48, 0x4b400000
	v_perm_b32 v49, v50, v49, s33
	v_perm_b32 v51, v52, v51, s34
	v_or_b32_e32 v126, v49, v51
	v_fmaak_f32 v53, v30, v48, 0x4b400000
	v_fmaak_f32 v54, v31, v48, 0x4b400000
	v_fmaak_f32 v55, v32, v48, 0x4b400000
	v_fmaak_f32 v46, v33, v48, 0x4b400000
	v_perm_b32 v53, v54, v53, s33
	v_perm_b32 v55, v46, v55, s34
	v_or_b32_e32 v127, v53, v55
	ds_write_b128 v38, v[124:127] offset:5120
	s_waitcnt vmcnt(0)
	ds_read_b128 v[18:21], v38 offset:0
	ds_read_b128 v[22:25], v38 offset:1024
	ds_read_b128 v[26:29], v38 offset:2048
	ds_read_b128 v[30:33], v38 offset:3072
	s_waitcnt lgkmcnt(0)
	s_mov_b32 m0, s35
	s_nop 0
	global_load_lds_dwordx4 v34, s[16:17] nt
	global_load_lds_dwordx4 v34, s[16:17] offset:1024 nt
	global_load_lds_dwordx4 v34, s[16:17] offset:2048 nt
	global_load_lds_dwordx4 v35, s[16:17] offset:3072 nt
	s_add_u32 s16, s16, 0x7d00
	s_addc_u32 s17, s17, 0
	v_cndmask_b32_e64 v30, 0, v30, s[18:19]
	v_cndmask_b32_e64 v31, 0, v31, s[18:19]
	v_cndmask_b32_e64 v32, 0, v32, s[18:19]
	v_cndmask_b32_e64 v33, 0, v33, s[18:19]
	v_max3_f32 v41, |v18|, |v19|, |v20|
	v_max3_f32 v42, |v21|, |v22|, |v23|
	v_max3_f32 v43, |v24|, |v25|, |v26|
	v_max3_f32 v44, |v27|, |v28|, |v29|
	v_max3_f32 v45, |v30|, |v31|, |v32|
	v_max3_f32 v41, v41, v42, |v33|
	v_max3_f32 v43, v43, v44, v45
	v_max_f32_e32 v41, v41, v43
	v_pk_add_f32 v[2:3], v[2:3], v[18:19]
	v_pk_add_f32 v[4:5], v[4:5], v[20:21]
	v_max_f32_dpp v41, v41, v41 quad_perm:[1,0,3,2] row_mask:0xf bank_mask:0xf
	v_pk_add_f32 v[6:7], v[6:7], v[22:23]
	v_pk_add_f32 v[8:9], v[8:9], v[24:25]
	v_max_f32_dpp v41, v41, v41 quad_perm:[2,3,0,1] row_mask:0xf bank_mask:0xf
	v_pk_add_f32 v[10:11], v[10:11], v[26:27]
	v_pk_add_f32 v[12:13], v[12:13], v[28:29]
	v_max_f32_dpp v41, v41, v41 row_half_mirror row_mask:0xf bank_mask:0xf
	v_pk_add_f32 v[14:15], v[14:15], v[30:31]
	v_pk_add_f32 v[16:17], v[16:17], v[32:33]
	v_max_f32_dpp v41, v41, v41 row_mirror row_mask:0xf bank_mask:0xf
	s_nop 1
	v_max_f32_dpp v41, v41, v41 row_bcast:15 row_mask:0xa bank_mask:0xf
	s_nop 1
	v_max_f32_dpp v41, v41, v41 row_bcast:31 row_mask:0xc bank_mask:0xf
	s_nop 1
	v_readlane_b32 s28, v41, 63
	s_nop 1
	v_div_scale_f32 v48, s[30:31], s28, s28, v47
	v_rcp_f32_e32 v49, v48
	s_nop 0
	v_fma_f32 v50, -v48, v49, 1.0
	v_fmac_f32_e32 v49, v50, v49
	v_mov_b32_e32 v50, s28
	v_div_scale_f32 v50, vcc, s32, v50, s32
	v_mul_f32_e32 v51, v50, v49
	v_fma_f32 v52, -v48, v51, v50
	v_fmac_f32_e32 v51, v52, v49
	v_fma_f32 v48, -v48, v51, v50
	v_div_fmas_f32 v48, v48, v49, v51
	v_div_fixup_f32 v48, v48, s28, v47
	v_cmp_gt_f32_e64 vcc, s28, 0
	v_writelane_b32 v40, s28, 19
	s_nop 0
	v_cndmask_b32_e32 v48, 0, v48, vcc
	v_fmaak_f32 v49, v18, v48, 0x4b400000
	v_fmaak_f32 v50, v19, v48, 0x4b400000
	v_fmaak_f32 v51, v20, v48, 0x4b400000
	v_fmaak_f32 v52, v21, v48, 0x4b400000
	v_perm_b32 v49, v50, v49, s33
	v_perm_b32 v51, v52, v51, s34
	v_or_b32_e32 v124, v49, v51
	v_fmaak_f32 v53, v22, v48, 0x4b400000
	v_fmaak_f32 v54, v23, v48, 0x4b400000
	v_fmaak_f32 v55, v24, v48, 0x4b400000
	v_fmaak_f32 v46, v25, v48, 0x4b400000
	v_perm_b32 v53, v54, v53, s33
	v_perm_b32 v55, v46, v55, s34
	v_or_b32_e32 v125, v53, v55
	v_fmaak_f32 v49, v26, v48, 0x4b400000
	v_fmaak_f32 v50, v27, v48, 0x4b400000
	v_fmaak_f32 v51, v28, v48, 0x4b400000
	v_fmaak_f32 v52, v29, v48, 0x4b400000
	v_perm_b32 v49, v50, v49, s33
	v_perm_b32 v51, v52, v51, s34
	v_or_b32_e32 v126, v49, v51
	v_fmaak_f32 v53, v30, v48, 0x4b400000
	v_fmaak_f32 v54, v31, v48, 0x4b400000
	v_fmaak_f32 v55, v32, v48, 0x4b400000
	v_fmaak_f32 v46, v33, v48, 0x4b400000
	v_perm_b32 v53, v54, v53, s33
	v_perm_b32 v55, v46, v55, s34
	v_or_b32_e32 v127, v53, v55
	ds_write_b128 v38, v[124:127] offset:6144
	s_waitcnt vmcnt(0)
	ds_read_b128 v[18:21], v38 offset:0
	ds_read_b128 v[22:25], v38 offset:1024
	ds_read_b128 v[26:29], v38 offset:2048
	ds_read_b128 v[30:33], v38 offset:3072
	s_waitcnt lgkmcnt(0)
	s_mov_b32 m0, s35
	s_nop 0
	global_load_lds_dwordx4 v34, s[16:17] nt
	global_load_lds_dwordx4 v34, s[16:17] offset:1024 nt
	global_load_lds_dwordx4 v34, s[16:17] offset:2048 nt
	global_load_lds_dwordx4 v35, s[16:17] offset:3072 nt
	s_add_u32 s16, s16, 0x7d00
	s_addc_u32 s17, s17, 0
	v_cndmask_b32_e64 v30, 0, v30, s[18:19]
	v_cndmask_b32_e64 v31, 0, v31, s[18:19]
	v_cndmask_b32_e64 v32, 0, v32, s[18:19]
	v_cndmask_b32_e64 v33, 0, v33, s[18:19]
	v_max3_f32 v41, |v18|, |v19|, |v20|
	v_max3_f32 v42, |v21|, |v22|, |v23|
	v_max3_f32 v43, |v24|, |v25|, |v26|
	v_max3_f32 v44, |v27|, |v28|, |v29|
	v_max3_f32 v45, |v30|, |v31|, |v32|
	v_max3_f32 v41, v41, v42, |v33|
	v_max3_f32 v43, v43, v44, v45
	v_max_f32_e32 v41, v41, v43
	v_pk_add_f32 v[2:3], v[2:3], v[18:19]
	v_pk_add_f32 v[4:5], v[4:5], v[20:21]
	v_max_f32_dpp v41, v41, v41 quad_perm:[1,0,3,2] row_mask:0xf bank_mask:0xf
	v_pk_add_f32 v[6:7], v[6:7], v[22:23]
	v_pk_add_f32 v[8:9], v[8:9], v[24:25]
	v_max_f32_dpp v41, v41, v41 quad_perm:[2,3,0,1] row_mask:0xf bank_mask:0xf
	v_pk_add_f32 v[10:11], v[10:11], v[26:27]
	v_pk_add_f32 v[12:13], v[12:13], v[28:29]
	v_max_f32_dpp v41, v41, v41 row_half_mirror row_mask:0xf bank_mask:0xf
	v_pk_add_f32 v[14:15], v[14:15], v[30:31]
	v_pk_add_f32 v[16:17], v[16:17], v[32:33]
	v_max_f32_dpp v41, v41, v41 row_mirror row_mask:0xf bank_mask:0xf
	s_nop 1
	v_max_f32_dpp v41, v41, v41 row_bcast:15 row_mask:0xa bank_mask:0xf
	s_nop 1
	v_max_f32_dpp v41, v41, v41 row_bcast:31 row_mask:0xc bank_mask:0xf
	s_nop 1
	v_readlane_b32 s28, v41, 63
	s_nop 1
	v_div_scale_f32 v48, s[30:31], s28, s28, v47
	v_rcp_f32_e32 v49, v48
	s_nop 0
	v_fma_f32 v50, -v48, v49, 1.0
	v_fmac_f32_e32 v49, v50, v49
	v_mov_b32_e32 v50, s28
	v_div_scale_f32 v50, vcc, s32, v50, s32
	v_mul_f32_e32 v51, v50, v49
	v_fma_f32 v52, -v48, v51, v50
	v_fmac_f32_e32 v51, v52, v49
	v_fma_f32 v48, -v48, v51, v50
	v_div_fmas_f32 v48, v48, v49, v51
	v_div_fixup_f32 v48, v48, s28, v47
	v_cmp_gt_f32_e64 vcc, s28, 0
	v_writelane_b32 v40, s28, 20
	s_nop 0
	v_cndmask_b32_e32 v48, 0, v48, vcc
	v_fmaak_f32 v49, v18, v48, 0x4b400000
	v_fmaak_f32 v50, v19, v48, 0x4b400000
	v_fmaak_f32 v51, v20, v48, 0x4b400000
	v_fmaak_f32 v52, v21, v48, 0x4b400000
	v_perm_b32 v49, v50, v49, s33
	v_perm_b32 v51, v52, v51, s34
	v_or_b32_e32 v124, v49, v51
	v_fmaak_f32 v53, v22, v48, 0x4b400000
	v_fmaak_f32 v54, v23, v48, 0x4b400000
	v_fmaak_f32 v55, v24, v48, 0x4b400000
	v_fmaak_f32 v46, v25, v48, 0x4b400000
	v_perm_b32 v53, v54, v53, s33
	v_perm_b32 v55, v46, v55, s34
	v_or_b32_e32 v125, v53, v55
	v_fmaak_f32 v49, v26, v48, 0x4b400000
	v_fmaak_f32 v50, v27, v48, 0x4b400000
	v_fmaak_f32 v51, v28, v48, 0x4b400000
	v_fmaak_f32 v52, v29, v48, 0x4b400000
	v_perm_b32 v49, v50, v49, s33
	v_perm_b32 v51, v52, v51, s34
	v_or_b32_e32 v126, v49, v51
	v_fmaak_f32 v53, v30, v48, 0x4b400000
	v_fmaak_f32 v54, v31, v48, 0x4b400000
	v_fmaak_f32 v55, v32, v48, 0x4b400000
	v_fmaak_f32 v46, v33, v48, 0x4b400000
	v_perm_b32 v53, v54, v53, s33
	v_perm_b32 v55, v46, v55, s34
	v_or_b32_e32 v127, v53, v55
	ds_write_b128 v38, v[124:127] offset:7168
	s_waitcnt vmcnt(0)
	ds_read_b128 v[18:21], v38 offset:0
	ds_read_b128 v[22:25], v38 offset:1024
	ds_read_b128 v[26:29], v38 offset:2048
	ds_read_b128 v[30:33], v38 offset:3072
	s_waitcnt lgkmcnt(0)
	s_mov_b32 m0, s35
	s_nop 0
	global_load_lds_dwordx4 v34, s[16:17] nt
	global_load_lds_dwordx4 v34, s[16:17] offset:1024 nt
	global_load_lds_dwordx4 v34, s[16:17] offset:2048 nt
	global_load_lds_dwordx4 v35, s[16:17] offset:3072 nt
	s_add_u32 s16, s16, 0x7d00
	s_addc_u32 s17, s17, 0
	v_cndmask_b32_e64 v30, 0, v30, s[18:19]
	v_cndmask_b32_e64 v31, 0, v31, s[18:19]
	v_cndmask_b32_e64 v32, 0, v32, s[18:19]
	v_cndmask_b32_e64 v33, 0, v33, s[18:19]
	v_max3_f32 v41, |v18|, |v19|, |v20|
	v_max3_f32 v42, |v21|, |v22|, |v23|
	v_max3_f32 v43, |v24|, |v25|, |v26|
	v_max3_f32 v44, |v27|, |v28|, |v29|
	v_max3_f32 v45, |v30|, |v31|, |v32|
	v_max3_f32 v41, v41, v42, |v33|
	v_max3_f32 v43, v43, v44, v45
	v_max_f32_e32 v41, v41, v43
	v_pk_add_f32 v[2:3], v[2:3], v[18:19]
	v_pk_add_f32 v[4:5], v[4:5], v[20:21]
	v_max_f32_dpp v41, v41, v41 quad_perm:[1,0,3,2] row_mask:0xf bank_mask:0xf
	v_pk_add_f32 v[6:7], v[6:7], v[22:23]
	v_pk_add_f32 v[8:9], v[8:9], v[24:25]
	v_max_f32_dpp v41, v41, v41 quad_perm:[2,3,0,1] row_mask:0xf bank_mask:0xf
	v_pk_add_f32 v[10:11], v[10:11], v[26:27]
	v_pk_add_f32 v[12:13], v[12:13], v[28:29]
	v_max_f32_dpp v41, v41, v41 row_half_mirror row_mask:0xf bank_mask:0xf
	v_pk_add_f32 v[14:15], v[14:15], v[30:31]
	v_pk_add_f32 v[16:17], v[16:17], v[32:33]
	v_max_f32_dpp v41, v41, v41 row_mirror row_mask:0xf bank_mask:0xf
	s_nop 1
	v_max_f32_dpp v41, v41, v41 row_bcast:15 row_mask:0xa bank_mask:0xf
	s_nop 1
	v_max_f32_dpp v41, v41, v41 row_bcast:31 row_mask:0xc bank_mask:0xf
	s_nop 1
	v_readlane_b32 s28, v41, 63
	s_nop 1
	v_div_scale_f32 v48, s[30:31], s28, s28, v47
	v_rcp_f32_e32 v49, v48
	s_nop 0
	v_fma_f32 v50, -v48, v49, 1.0
	v_fmac_f32_e32 v49, v50, v49
	v_mov_b32_e32 v50, s28
	v_div_scale_f32 v50, vcc, s32, v50, s32
	v_mul_f32_e32 v51, v50, v49
	v_fma_f32 v52, -v48, v51, v50
	v_fmac_f32_e32 v51, v52, v49
	v_fma_f32 v48, -v48, v51, v50
	v_div_fmas_f32 v48, v48, v49, v51
	v_div_fixup_f32 v48, v48, s28, v47
	v_cmp_gt_f32_e64 vcc, s28, 0
	v_writelane_b32 v40, s28, 21
	s_nop 0
	v_cndmask_b32_e32 v48, 0, v48, vcc
	v_fmaak_f32 v49, v18, v48, 0x4b400000
	v_fmaak_f32 v50, v19, v48, 0x4b400000
	v_fmaak_f32 v51, v20, v48, 0x4b400000
	v_fmaak_f32 v52, v21, v48, 0x4b400000
	v_perm_b32 v49, v50, v49, s33
	v_perm_b32 v51, v52, v51, s34
	v_or_b32_e32 v49, v49, v51
	s_add_u32 s20, s20, 0x5400
	s_addc_u32 s21, s21, 0
	s_add_u32 s22, s22, 0x5400
	s_addc_u32 s23, s23, 0
	s_add_u32 s24, s24, 0x5400
	s_addc_u32 s25, s25, 0
	s_add_u32 s26, s26, 0x5400
	s_addc_u32 s27, s27, 0
	global_store_dword v39, v49, s[20:21]
	v_fmaak_f32 v53, v22, v48, 0x4b400000
	v_fmaak_f32 v54, v23, v48, 0x4b400000
	v_fmaak_f32 v55, v24, v48, 0x4b400000
	v_fmaak_f32 v46, v25, v48, 0x4b400000
	v_perm_b32 v53, v54, v53, s33
	v_perm_b32 v55, v46, v55, s34
	v_or_b32_e32 v53, v53, v55
	global_store_dword v39, v53, s[22:23]
	v_fmaak_f32 v49, v26, v48, 0x4b400000
	v_fmaak_f32 v50, v27, v48, 0x4b400000
	v_fmaak_f32 v51, v28, v48, 0x4b400000
	v_fmaak_f32 v52, v29, v48, 0x4b400000
	v_perm_b32 v49, v50, v49, s33
	v_perm_b32 v51, v52, v51, s34
	v_or_b32_e32 v49, v49, v51
	global_store_dword v39, v49, s[24:25]
	v_fmaak_f32 v53, v30, v48, 0x4b400000
	v_fmaak_f32 v54, v31, v48, 0x4b400000
	v_fmaak_f32 v55, v32, v48, 0x4b400000
	v_fmaak_f32 v46, v33, v48, 0x4b400000
	v_perm_b32 v53, v54, v53, s33
	v_perm_b32 v55, v46, v55, s34
	v_or_b32_e32 v53, v53, v55
	global_store_dword v39, v53, s[26:27]
	s_waitcnt vmcnt(4)
	ds_read_b128 v[18:21], v38 offset:0
	ds_read_b128 v[22:25], v38 offset:1024
	ds_read_b128 v[26:29], v38 offset:2048
	ds_read_b128 v[30:33], v38 offset:3072
	s_waitcnt lgkmcnt(0)
	s_mov_b32 m0, s35
	s_nop 0
	global_load_lds_dwordx4 v34, s[16:17] nt
	global_load_lds_dwordx4 v34, s[16:17] offset:1024 nt
	global_load_lds_dwordx4 v34, s[16:17] offset:2048 nt
	global_load_lds_dwordx4 v35, s[16:17] offset:3072 nt
	s_add_u32 s16, s16, 0x7d00
	s_addc_u32 s17, s17, 0
	v_cndmask_b32_e64 v30, 0, v30, s[18:19]
	v_cndmask_b32_e64 v31, 0, v31, s[18:19]
	v_cndmask_b32_e64 v32, 0, v32, s[18:19]
	v_cndmask_b32_e64 v33, 0, v33, s[18:19]
	v_max3_f32 v41, |v18|, |v19|, |v20|
	v_max3_f32 v42, |v21|, |v22|, |v23|
	v_max3_f32 v43, |v24|, |v25|, |v26|
	v_max3_f32 v44, |v27|, |v28|, |v29|
	v_max3_f32 v45, |v30|, |v31|, |v32|
	v_max3_f32 v41, v41, v42, |v33|
	v_max3_f32 v43, v43, v44, v45
	v_max_f32_e32 v41, v41, v43
	v_pk_add_f32 v[2:3], v[2:3], v[18:19]
	v_pk_add_f32 v[4:5], v[4:5], v[20:21]
	v_max_f32_dpp v41, v41, v41 quad_perm:[1,0,3,2] row_mask:0xf bank_mask:0xf
	v_pk_add_f32 v[6:7], v[6:7], v[22:23]
	v_pk_add_f32 v[8:9], v[8:9], v[24:25]
	v_max_f32_dpp v41, v41, v41 quad_perm:[2,3,0,1] row_mask:0xf bank_mask:0xf
	v_pk_add_f32 v[10:11], v[10:11], v[26:27]
	v_pk_add_f32 v[12:13], v[12:13], v[28:29]
	v_max_f32_dpp v41, v41, v41 row_half_mirror row_mask:0xf bank_mask:0xf
	v_pk_add_f32 v[14:15], v[14:15], v[30:31]
	v_pk_add_f32 v[16:17], v[16:17], v[32:33]
	v_max_f32_dpp v41, v41, v41 row_mirror row_mask:0xf bank_mask:0xf
	s_nop 1
	v_max_f32_dpp v41, v41, v41 row_bcast:15 row_mask:0xa bank_mask:0xf
	s_nop 1
	v_max_f32_dpp v41, v41, v41 row_bcast:31 row_mask:0xc bank_mask:0xf
	s_nop 1
	v_readlane_b32 s28, v41, 63
	s_nop 1
	v_div_scale_f32 v48, s[30:31], s28, s28, v47
	v_rcp_f32_e32 v49, v48
	s_nop 0
	v_fma_f32 v50, -v48, v49, 1.0
	v_fmac_f32_e32 v49, v50, v49
	v_mov_b32_e32 v50, s28
	v_div_scale_f32 v50, vcc, s32, v50, s32
	v_mul_f32_e32 v51, v50, v49
	v_fma_f32 v52, -v48, v51, v50
	v_fmac_f32_e32 v51, v52, v49
	v_fma_f32 v48, -v48, v51, v50
	v_div_fmas_f32 v48, v48, v49, v51
	v_div_fixup_f32 v48, v48, s28, v47
	v_cmp_gt_f32_e64 vcc, s28, 0
	v_writelane_b32 v40, s28, 22
	s_nop 0
	v_cndmask_b32_e32 v48, 0, v48, vcc
	v_fmaak_f32 v49, v18, v48, 0x4b400000
	v_fmaak_f32 v50, v19, v48, 0x4b400000
	v_fmaak_f32 v51, v20, v48, 0x4b400000
	v_fmaak_f32 v52, v21, v48, 0x4b400000
	v_perm_b32 v49, v50, v49, s33
	v_perm_b32 v51, v52, v51, s34
	v_or_b32_e32 v49, v49, v51
	s_add_u32 s20, s20, 0x400
	s_addc_u32 s21, s21, 0
	s_add_u32 s22, s22, 0x400
	s_addc_u32 s23, s23, 0
	s_add_u32 s24, s24, 0x400
	s_addc_u32 s25, s25, 0
	s_add_u32 s26, s26, 0x400
	s_addc_u32 s27, s27, 0
	global_store_dword v39, v49, s[20:21]
	v_fmaak_f32 v53, v22, v48, 0x4b400000
	v_fmaak_f32 v54, v23, v48, 0x4b400000
	v_fmaak_f32 v55, v24, v48, 0x4b400000
	v_fmaak_f32 v46, v25, v48, 0x4b400000
	v_perm_b32 v53, v54, v53, s33
	v_perm_b32 v55, v46, v55, s34
	v_or_b32_e32 v53, v53, v55
	global_store_dword v39, v53, s[22:23]
	v_fmaak_f32 v49, v26, v48, 0x4b400000
	v_fmaak_f32 v50, v27, v48, 0x4b400000
	v_fmaak_f32 v51, v28, v48, 0x4b400000
	v_fmaak_f32 v52, v29, v48, 0x4b400000
	v_perm_b32 v49, v50, v49, s33
	v_perm_b32 v51, v52, v51, s34
	v_or_b32_e32 v49, v49, v51
	global_store_dword v39, v49, s[24:25]
	v_fmaak_f32 v53, v30, v48, 0x4b400000
	v_fmaak_f32 v54, v31, v48, 0x4b400000
	v_fmaak_f32 v55, v32, v48, 0x4b400000
	v_fmaak_f32 v46, v33, v48, 0x4b400000
	v_perm_b32 v53, v54, v53, s33
	v_perm_b32 v55, v46, v55, s34
	v_or_b32_e32 v53, v53, v55
	global_store_dword v39, v53, s[26:27]
	s_waitcnt vmcnt(4)
	ds_read_b128 v[18:21], v38 offset:0
	ds_read_b128 v[22:25], v38 offset:1024
	ds_read_b128 v[26:29], v38 offset:2048
	ds_read_b128 v[30:33], v38 offset:3072
	s_waitcnt lgkmcnt(0)
	s_cmp_eq_u32 s29, 1
	s_cbranch_scc0 .Lk1_nodma24
	s_mov_b32 m0, s35
	s_nop 0
	global_load_lds_dwordx4 v34, s[16:17] nt
	global_load_lds_dwordx4 v34, s[16:17] offset:1024 nt
	global_load_lds_dwordx4 v34, s[16:17] offset:2048 nt
	global_load_lds_dwordx4 v35, s[16:17] offset:3072 nt
	s_add_u32 s16, s16, 0x7d00
	s_addc_u32 s17, s17, 0
.Lk1_nodma24:
	v_cndmask_b32_e64 v30, 0, v30, s[18:19]
	v_cndmask_b32_e64 v31, 0, v31, s[18:19]
	v_cndmask_b32_e64 v32, 0, v32, s[18:19]
	v_cndmask_b32_e64 v33, 0, v33, s[18:19]
	v_max3_f32 v41, |v18|, |v19|, |v20|
	v_max3_f32 v42, |v21|, |v22|, |v23|
	v_max3_f32 v43, |v24|, |v25|, |v26|
	v_max3_f32 v44, |v27|, |v28|, |v29|
	v_max3_f32 v45, |v30|, |v31|, |v32|
	v_max3_f32 v41, v41, v42, |v33|
	v_max3_f32 v43, v43, v44, v45
	v_max_f32_e32 v41, v41, v43
	v_pk_add_f32 v[2:3], v[2:3], v[18:19]
	v_pk_add_f32 v[4:5], v[4:5], v[20:21]
	v_max_f32_dpp v41, v41, v41 quad_perm:[1,0,3,2] row_mask:0xf bank_mask:0xf
	v_pk_add_f32 v[6:7], v[6:7], v[22:23]
	v_pk_add_f32 v[8:9], v[8:9], v[24:25]
	v_max_f32_dpp v41, v41, v41 quad_perm:[2,3,0,1] row_mask:0xf bank_mask:0xf
	v_pk_add_f32 v[10:11], v[10:11], v[26:27]
	v_pk_add_f32 v[12:13], v[12:13], v[28:29]
	v_max_f32_dpp v41, v41, v41 row_half_mirror row_mask:0xf bank_mask:0xf
	v_pk_add_f32 v[14:15], v[14:15], v[30:31]
	v_pk_add_f32 v[16:17], v[16:17], v[32:33]
	v_max_f32_dpp v41, v41, v41 row_mirror row_mask:0xf bank_mask:0xf
	s_nop 1
	v_max_f32_dpp v41, v41, v41 row_bcast:15 row_mask:0xa bank_mask:0xf
	s_nop 1
	v_max_f32_dpp v41, v41, v41 row_bcast:31 row_mask:0xc bank_mask:0xf
	s_nop 1
	v_readlane_b32 s28, v41, 63
	s_nop 1
	v_div_scale_f32 v48, s[30:31], s28, s28, v47
	v_rcp_f32_e32 v49, v48
	s_nop 0
	v_fma_f32 v50, -v48, v49, 1.0
	v_fmac_f32_e32 v49, v50, v49
	v_mov_b32_e32 v50, s28
	v_div_scale_f32 v50, vcc, s32, v50, s32
	v_mul_f32_e32 v51, v50, v49
	v_fma_f32 v52, -v48, v51, v50
	v_fmac_f32_e32 v51, v52, v49
	v_fma_f32 v48, -v48, v51, v50
	v_div_fmas_f32 v48, v48, v49, v51
	v_div_fixup_f32 v48, v48, s28, v47
	v_cmp_gt_f32_e64 vcc, s28, 0
	v_writelane_b32 v40, s28, 23
	s_nop 0
	v_cndmask_b32_e32 v48, 0, v48, vcc
	v_fmaak_f32 v49, v18, v48, 0x4b400000
	v_fmaak_f32 v50, v19, v48, 0x4b400000
	v_fmaak_f32 v51, v20, v48, 0x4b400000
	v_fmaak_f32 v52, v21, v48, 0x4b400000
	v_perm_b32 v49, v50, v49, s33
	v_perm_b32 v51, v52, v51, s34
	v_or_b32_e32 v49, v49, v51
	s_add_u32 s20, s20, 0x400
	s_addc_u32 s21, s21, 0
	s_add_u32 s22, s22, 0x400
	s_addc_u32 s23, s23, 0
	s_add_u32 s24, s24, 0x400
	s_addc_u32 s25, s25, 0
	s_add_u32 s26, s26, 0x400
	s_addc_u32 s27, s27, 0
	global_store_dword v39, v49, s[20:21]
	v_fmaak_f32 v53, v22, v48, 0x4b400000
	v_fmaak_f32 v54, v23, v48, 0x4b400000
	v_fmaak_f32 v55, v24, v48, 0x4b400000
	v_fmaak_f32 v46, v25, v48, 0x4b400000
	v_perm_b32 v53, v54, v53, s33
	v_perm_b32 v55, v46, v55, s34
	v_or_b32_e32 v53, v53, v55
	global_store_dword v39, v53, s[22:23]
	v_fmaak_f32 v49, v26, v48, 0x4b400000
	v_fmaak_f32 v50, v27, v48, 0x4b400000
	v_fmaak_f32 v51, v28, v48, 0x4b400000
	v_fmaak_f32 v52, v29, v48, 0x4b400000
	v_perm_b32 v49, v50, v49, s33
	v_perm_b32 v51, v52, v51, s34
	v_or_b32_e32 v49, v49, v51
	global_store_dword v39, v49, s[24:25]
	v_fmaak_f32 v53, v30, v48, 0x4b400000
	v_fmaak_f32 v54, v31, v48, 0x4b400000
	v_fmaak_f32 v55, v32, v48, 0x4b400000
	v_fmaak_f32 v46, v33, v48, 0x4b400000
	v_perm_b32 v53, v54, v53, s33
	v_perm_b32 v55, v46, v55, s34
	v_or_b32_e32 v53, v53, v55
	global_store_dword v39, v53, s[26:27]
	s_cmp_eq_u32 s29, 1
	s_cbranch_scc0 .Lk1_flush
	s_waitcnt vmcnt(4)
	ds_read_b128 v[18:21], v38 offset:0
	ds_read_b128 v[22:25], v38 offset:1024
	ds_read_b128 v[26:29], v38 offset:2048
	ds_read_b128 v[30:33], v38 offset:3072
	s_waitcnt lgkmcnt(0)
	v_cndmask_b32_e64 v30, 0, v30, s[18:19]
	v_cndmask_b32_e64 v31, 0, v31, s[18:19]
	v_cndmask_b32_e64 v32, 0, v32, s[18:19]
	v_cndmask_b32_e64 v33, 0, v33, s[18:19]
	v_max3_f32 v41, |v18|, |v19|, |v20|
	v_max3_f32 v42, |v21|, |v22|, |v23|
	v_max3_f32 v43, |v24|, |v25|, |v26|
	v_max3_f32 v44, |v27|, |v28|, |v29|
	v_max3_f32 v45, |v30|, |v31|, |v32|
	v_max3_f32 v41, v41, v42, |v33|
	v_max3_f32 v43, v43, v44, v45
	v_max_f32_e32 v41, v41, v43
	v_pk_add_f32 v[2:3], v[2:3], v[18:19]
	v_pk_add_f32 v[4:5], v[4:5], v[20:21]
	v_max_f32_dpp v41, v41, v41 quad_perm:[1,0,3,2] row_mask:0xf bank_mask:0xf
	v_pk_add_f32 v[6:7], v[6:7], v[22:23]
	v_pk_add_f32 v[8:9], v[8:9], v[24:25]
	v_max_f32_dpp v41, v41, v41 quad_perm:[2,3,0,1] row_mask:0xf bank_mask:0xf
	v_pk_add_f32 v[10:11], v[10:11], v[26:27]
	v_pk_add_f32 v[12:13], v[12:13], v[28:29]
	v_max_f32_dpp v41, v41, v41 row_half_mirror row_mask:0xf bank_mask:0xf
	v_pk_add_f32 v[14:15], v[14:15], v[30:31]
	v_pk_add_f32 v[16:17], v[16:17], v[32:33]
	v_max_f32_dpp v41, v41, v41 row_mirror row_mask:0xf bank_mask:0xf
	s_nop 1
	v_max_f32_dpp v41, v41, v41 row_bcast:15 row_mask:0xa bank_mask:0xf
	s_nop 1
	v_max_f32_dpp v41, v41, v41 row_bcast:31 row_mask:0xc bank_mask:0xf
	s_nop 1
	v_readlane_b32 s28, v41, 63
	s_nop 1
	v_div_scale_f32 v48, s[30:31], s28, s28, v47
	v_rcp_f32_e32 v49, v48
	s_nop 0
	v_fma_f32 v50, -v48, v49, 1.0
	v_fmac_f32_e32 v49, v50, v49
	v_mov_b32_e32 v50, s28
	v_div_scale_f32 v50, vcc, s32, v50, s32
	v_mul_f32_e32 v51, v50, v49
	v_fma_f32 v52, -v48, v51, v50
	v_fmac_f32_e32 v51, v52, v49
	v_fma_f32 v48, -v48, v51, v50
	v_div_fmas_f32 v48, v48, v49, v51
	v_div_fixup_f32 v48, v48, s28, v47
	v_cmp_gt_f32_e64 vcc, s28, 0
	v_writelane_b32 v40, s28, 24
	s_nop 0
	v_cndmask_b32_e32 v48, 0, v48, vcc
	v_fmaak_f32 v49, v18, v48, 0x4b400000
	v_fmaak_f32 v50, v19, v48, 0x4b400000
	v_fmaak_f32 v51, v20, v48, 0x4b400000
	v_fmaak_f32 v52, v21, v48, 0x4b400000
	v_perm_b32 v49, v50, v49, s33
	v_perm_b32 v51, v52, v51, s34
	v_or_b32_e32 v49, v49, v51
	s_add_u32 s20, s20, 0x400
	s_addc_u32 s21, s21, 0
	s_add_u32 s22, s22, 0x400
	s_addc_u32 s23, s23, 0
	s_add_u32 s24, s24, 0x400
	s_addc_u32 s25, s25, 0
	s_add_u32 s26, s26, 0x400
	s_addc_u32 s27, s27, 0
	global_store_dword v39, v49, s[20:21]
	v_fmaak_f32 v53, v22, v48, 0x4b400000
	v_fmaak_f32 v54, v23, v48, 0x4b400000
	v_fmaak_f32 v55, v24, v48, 0x4b400000
	v_fmaak_f32 v46, v25, v48, 0x4b400000
	v_perm_b32 v53, v54, v53, s33
	v_perm_b32 v55, v46, v55, s34
	v_or_b32_e32 v53, v53, v55
	global_store_dword v39, v53, s[22:23]
	v_fmaak_f32 v49, v26, v48, 0x4b400000
	v_fmaak_f32 v50, v27, v48, 0x4b400000
	v_fmaak_f32 v51, v28, v48, 0x4b400000
	v_fmaak_f32 v52, v29, v48, 0x4b400000
	v_perm_b32 v49, v50, v49, s33
	v_perm_b32 v51, v52, v51, s34
	v_or_b32_e32 v49, v49, v51
	global_store_dword v39, v49, s[24:25]
	v_fmaak_f32 v53, v30, v48, 0x4b400000
	v_fmaak_f32 v54, v31, v48, 0x4b400000
	v_fmaak_f32 v55, v32, v48, 0x4b400000
	v_fmaak_f32 v46, v33, v48, 0x4b400000
	v_perm_b32 v53, v54, v53, s33
	v_perm_b32 v55, v46, v55, s34
	v_or_b32_e32 v53, v53, v55
	global_store_dword v39, v53, s[26:27]
.Lk1_flush:
	s_add_u32 s20, s40, 0x0
	s_addc_u32 s21, s41, 0
	s_add_u32 s22, s20, 0x186a000
	s_addc_u32 s23, s21, 0
	s_add_u32 s24, s22, 0x186a000
	s_addc_u32 s25, s23, 0
	s_add_u32 s26, s24, 0x186a000
	s_addc_u32 s27, s25, 0
	global_store_dword v39, v56, s[20:21] sc1
	global_store_dword v39, v57, s[22:23] sc1
	global_store_dword v39, v58, s[24:25] sc1
	global_store_dword v39, v59, s[26:27] sc1
	global_store_dword v39, v60, s[20:21] offset:1024 sc1
	global_store_dword v39, v61, s[22:23] offset:1024 sc1
	global_store_dword v39, v62, s[24:25] offset:1024 sc1
	global_store_dword v39, v63, s[26:27] offset:1024 sc1
	global_store_dword v39, v64, s[20:21] offset:2048 sc1
	global_store_dword v39, v65, s[22:23] offset:2048 sc1
	global_store_dword v39, v66, s[24:25] offset:2048 sc1
	global_store_dword v39, v67, s[26:27] offset:2048 sc1
	global_store_dword v39, v68, s[20:21] offset:3072 sc1
	global_store_dword v39, v69, s[22:23] offset:3072 sc1
	global_store_dword v39, v70, s[24:25] offset:3072 sc1
	global_store_dword v39, v71, s[26:27] offset:3072 sc1
	s_add_u32 s20, s20, 0x1000
	s_addc_u32 s21, s21, 0
	s_add_u32 s22, s22, 0x1000
	s_addc_u32 s23, s23, 0
	s_add_u32 s24, s24, 0x1000
	s_addc_u32 s25, s25, 0
	s_add_u32 s26, s26, 0x1000
	s_addc_u32 s27, s27, 0
	global_store_dword v39, v72, s[20:21] sc1
	global_store_dword v39, v73, s[22:23] sc1
	global_store_dword v39, v74, s[24:25] sc1
	global_store_dword v39, v75, s[26:27] sc1
	global_store_dword v39, v76, s[20:21] offset:1024 sc1
	global_store_dword v39, v77, s[22:23] offset:1024 sc1
	global_store_dword v39, v78, s[24:25] offset:1024 sc1
	global_store_dword v39, v79, s[26:27] offset:1024 sc1
	global_store_dword v39, v80, s[20:21] offset:2048 sc1
	global_store_dword v39, v81, s[22:23] offset:2048 sc1
	global_store_dword v39, v82, s[24:25] offset:2048 sc1
	global_store_dword v39, v83, s[26:27] offset:2048 sc1
	global_store_dword v39, v84, s[20:21] offset:3072 sc1
	global_store_dword v39, v85, s[22:23] offset:3072 sc1
	global_store_dword v39, v86, s[24:25] offset:3072 sc1
	global_store_dword v39, v87, s[26:27] offset:3072 sc1
	s_add_u32 s20, s20, 0x1000
	s_addc_u32 s21, s21, 0
	s_add_u32 s22, s22, 0x1000
	s_addc_u32 s23, s23, 0
	s_add_u32 s24, s24, 0x1000
	s_addc_u32 s25, s25, 0
	s_add_u32 s26, s26, 0x1000
	s_addc_u32 s27, s27, 0
	global_store_dword v39, v88, s[20:21] sc1
	global_store_dword v39, v89, s[22:23] sc1
	global_store_dword v39, v90, s[24:25] sc1
	global_store_dword v39, v91, s[26:27] sc1
	global_store_dword v39, v92, s[20:21] offset:1024 sc1
	global_store_dword v39, v93, s[22:23] offset:1024 sc1
	global_store_dword v39, v94, s[24:25] offset:1024 sc1
	global_store_dword v39, v95, s[26:27] offset:1024 sc1
	global_store_dword v39, v96, s[20:21] offset:2048 sc1
	global_store_dword v39, v97, s[22:23] offset:2048 sc1
	global_store_dword v39, v98, s[24:25] offset:2048 sc1
	global_store_dword v39, v99, s[26:27] offset:2048 sc1
	global_store_dword v39, v100, s[20:21] offset:3072 sc1
	global_store_dword v39, v101, s[22:23] offset:3072 sc1
	global_store_dword v39, v102, s[24:25] offset:3072 sc1
	global_store_dword v39, v103, s[26:27] offset:3072 sc1
	s_add_u32 s20, s20, 0x1000
	s_addc_u32 s21, s21, 0
	s_add_u32 s22, s22, 0x1000
	s_addc_u32 s23, s23, 0
	s_add_u32 s24, s24, 0x1000
	s_addc_u32 s25, s25, 0
	s_add_u32 s26, s26, 0x1000
	s_addc_u32 s27, s27, 0
	global_store_dword v39, v104, s[20:21] sc1
	global_store_dword v39, v105, s[22:23] sc1
	global_store_dword v39, v106, s[24:25] sc1
	global_store_dword v39, v107, s[26:27] sc1
	global_store_dword v39, v108, s[20:21] offset:1024 sc1
	global_store_dword v39, v109, s[22:23] offset:1024 sc1
	global_store_dword v39, v110, s[24:25] offset:1024 sc1
	global_store_dword v39, v111, s[26:27] offset:1024 sc1
	global_store_dword v39, v112, s[20:21] offset:2048 sc1
	global_store_dword v39, v113, s[22:23] offset:2048 sc1
	global_store_dword v39, v114, s[24:25] offset:2048 sc1
	global_store_dword v39, v115, s[26:27] offset:2048 sc1
	global_store_dword v39, v116, s[20:21] offset:3072 sc1
	global_store_dword v39, v117, s[22:23] offset:3072 sc1
	global_store_dword v39, v118, s[24:25] offset:3072 sc1
	global_store_dword v39, v119, s[26:27] offset:3072 sc1
	s_add_u32 s20, s20, 0x1000
	s_addc_u32 s21, s21, 0
	s_add_u32 s22, s22, 0x1000
	s_addc_u32 s23, s23, 0
	s_add_u32 s24, s24, 0x1000
	s_addc_u32 s25, s25, 0
	s_add_u32 s26, s26, 0x1000
	s_addc_u32 s27, s27, 0
	global_store_dword v39, v120, s[20:21] sc1
	global_store_dword v39, v121, s[22:23] sc1
	global_store_dword v39, v122, s[24:25] sc1
	global_store_dword v39, v123, s[26:27] sc1
	ds_read_b128 v[56:59], v38 offset:4096
	ds_read_b128 v[60:63], v38 offset:5120
	ds_read_b128 v[64:67], v38 offset:6144
	ds_read_b128 v[68:71], v38 offset:7168
	s_waitcnt lgkmcnt(0)
	global_store_dword v39, v56, s[20:21] offset:1024 sc1
	global_store_dword v39, v57, s[22:23] offset:1024 sc1
	global_store_dword v39, v58, s[24:25] offset:1024 sc1
	global_store_dword v39, v59, s[26:27] offset:1024 sc1
	global_store_dword v39, v60, s[20:21] offset:2048 sc1
	global_store_dword v39, v61, s[22:23] offset:2048 sc1
	global_store_dword v39, v62, s[24:25] offset:2048 sc1
	global_store_dword v39, v63, s[26:27] offset:2048 sc1
	global_store_dword v39, v64, s[20:21] offset:3072 sc1
	global_store_dword v39, v65, s[22:23] offset:3072 sc1
	global_store_dword v39, v66, s[24:25] offset:3072 sc1
	global_store_dword v39, v67, s[26:27] offset:3072 sc1
	s_add_u32 s20, s20, 0x1000
	s_addc_u32 s21, s21, 0
	s_add_u32 s22, s22, 0x1000
	s_addc_u32 s23, s23, 0
	s_add_u32 s24, s24, 0x1000
	s_addc_u32 s25, s25, 0
	s_add_u32 s26, s26, 0x1000
	s_addc_u32 s27, s27, 0
	global_store_dword v39, v68, s[20:21] sc1
	global_store_dword v39, v69, s[22:23] sc1
	global_store_dword v39, v70, s[24:25] sc1
	global_store_dword v39, v71, s[26:27] sc1
	v_mul_f32_e32 v40, 0x3c010204, v40
	v_lshlrev_b32_e32 v41, 5, v1
	s_add_u32 s15, s12, s14
	s_lshl_b32 s15, s15, 2
	s_add_u32 s8, s8, s15
	s_addc_u32 s9, s9, 0
	s_add_u32 s15, s29, 24
	v_cmp_gt_u32_e32 vcc, s15, v1
	s_and_saveexec_b64 s[38:39], vcc
	global_store_dword v41, v40, s[8:9]
	s_mov_b64 exec, s[38:39]
	s_lshl_b32 s15, s14, 12
	v_add_u32_e32 v41, s15, v34
	s_barrier
	ds_write_b128 v41, v[2:5]
	ds_write_b128 v41, v[6:9] offset:1024
	ds_write_b128 v41, v[10:13] offset:2048
	ds_write_b128 v41, v[14:17] offset:3072
	s_waitcnt lgkmcnt(0)
	s_barrier
	s_movk_i32 s15, 0x100
	v_cmp_gt_u32_e32 vcc, s15, v0
	s_and_saveexec_b64 s[38:39], vcc
	s_cbranch_execz .Lk1_end
	v_lshlrev_b32_e32 v16, 4, v0
	ds_read_b128 v[2:5], v16
	ds_read_b128 v[18:21], v16 offset:4096
	ds_read_b128 v[22:25], v16 offset:8192
	ds_read_b128 v[26:29], v16 offset:12288
	ds_read_b128 v[30:33], v16 offset:16384
	ds_read_b128 v[34:37], v16 offset:20480
	ds_read_b128 v[38:41], v16 offset:24576
	ds_read_b128 v[42:45], v16 offset:28672
	s_waitcnt lgkmcnt(6)
	v_pk_add_f32 v[2:3], v[2:3], v[18:19]
	v_pk_add_f32 v[4:5], v[4:5], v[20:21]
	s_waitcnt lgkmcnt(5)
	v_pk_add_f32 v[2:3], v[2:3], v[22:23]
	v_pk_add_f32 v[4:5], v[4:5], v[24:25]
	s_waitcnt lgkmcnt(4)
	v_pk_add_f32 v[2:3], v[2:3], v[26:27]
	v_pk_add_f32 v[4:5], v[4:5], v[28:29]
	s_waitcnt lgkmcnt(3)
	v_pk_add_f32 v[2:3], v[2:3], v[30:31]
	v_pk_add_f32 v[4:5], v[4:5], v[32:33]
	s_waitcnt lgkmcnt(2)
	v_pk_add_f32 v[2:3], v[2:3], v[34:35]
	v_pk_add_f32 v[4:5], v[4:5], v[36:37]
	s_waitcnt lgkmcnt(1)
	v_pk_add_f32 v[2:3], v[2:3], v[38:39]
	v_pk_add_f32 v[4:5], v[4:5], v[40:41]
	s_waitcnt lgkmcnt(0)
	v_pk_add_f32 v[2:3], v[2:3], v[42:43]
	v_pk_add_f32 v[4:5], v[4:5], v[44:45]
	s_lshl_b32 s15, s2, 12
	s_add_u32 s10, s10, s15
	s_addc_u32 s11, s11, 0
	global_store_dwordx4 v16, v[2:5], s[10:11]
